# baseline (speedup 1.0000x reference)
.LBB8_2:
	v_add_u32_e32 v65, 0x100, v0
	v_mov_b32_e32 v67, 0
	v_add_u32_e32 v129, 0x200, v0
	v_mov_b32_e32 v131, 0
	v_mul_u32_u24_sdwa v2, v1, s21 dst_sel:DWORD dst_unused:UNUSED_PAD src0_sel:WORD_0 src1_sel:DWORD
	v_lshrrev_b32_e32 v42, 22, v2
	v_mul_lo_u16_e32 v2, 0x60, v42
	v_mul_u32_u24_e32 v4, 0x300, v42
	v_sub_u16_e32 v43, v1, v2
	v_lshlrev_b32_e32 v2, 2, v4
	v_add_u32_e32 v4, s20, v43
	v_ashrrev_i32_e32 v5, 31, v4
	v_lshlrev_b64 v[4:5], 2, v[4:5]
	s_waitcnt lgkmcnt(0)
	v_lshl_add_u64 v[6:7], s[4:5], 0, v[4:5]
	v_lshl_add_u64 v[8:9], s[6:7], 0, v[4:5]
	v_lshl_add_u64 v[6:7], v[6:7], 0, v[2:3]
	global_load_dword v44, v[8:9], off
	v_add_co_u32_e32 v8, vcc, s22, v6
	v_mul_u32_u24_e32 v12, 0x60000, v42
	s_nop 0
	v_addc_co_u32_e32 v9, vcc, 0, v7, vcc
	v_lshlrev_b32_e32 v2, 2, v12
	v_add_co_u32_e32 v12, vcc, s23, v6
	v_lshl_add_u64 v[40:41], s[16:17], 0, v[2:3]
	s_nop 0
	v_addc_co_u32_e32 v13, vcc, 0, v7, vcc
	v_add_co_u32_e32 v14, vcc, s24, v6
	v_lshl_add_u64 v[10:11], s[12:13], 0, v[4:5]
	s_nop 0
	v_addc_co_u32_e32 v15, vcc, 0, v7, vcc
	v_add_co_u32_e32 v16, vcc, s25, v6
	v_lshl_add_u64 v[4:5], v[40:41], 0, v[4:5]
	s_nop 0
	v_addc_co_u32_e32 v17, vcc, 0, v7, vcc
	v_add_co_u32_e32 v18, vcc, s26, v6
	s_nop 1
	v_addc_co_u32_e32 v19, vcc, 0, v7, vcc
	v_add_co_u32_e32 v20, vcc, s27, v6
	s_nop 1
	v_addc_co_u32_e32 v21, vcc, 0, v7, vcc
	v_add_co_u32_e32 v22, vcc, s28, v6
	s_nop 1
	v_addc_co_u32_e32 v23, vcc, 0, v7, vcc
	v_add_co_u32_e32 v24, vcc, s29, v6
	s_nop 1
	v_addc_co_u32_e32 v25, vcc, 0, v7, vcc
	v_add_co_u32_e32 v26, vcc, s30, v6
	s_nop 1
	v_addc_co_u32_e32 v27, vcc, 0, v7, vcc
	v_add_co_u32_e32 v28, vcc, s31, v6
	s_nop 1
	v_addc_co_u32_e32 v29, vcc, 0, v7, vcc
	v_add_co_u32_e32 v30, vcc, s33, v6
	s_nop 1
	v_addc_co_u32_e32 v31, vcc, 0, v7, vcc
	v_add_co_u32_e32 v32, vcc, s34, v6
	s_nop 1
	v_addc_co_u32_e32 v33, vcc, 0, v7, vcc
	v_add_co_u32_e32 v34, vcc, s35, v6
	s_nop 1
	v_addc_co_u32_e32 v35, vcc, 0, v7, vcc
	v_add_co_u32_e32 v36, vcc, s36, v6
	s_nop 1
	v_addc_co_u32_e32 v37, vcc, 0, v7, vcc
	v_add_co_u32_e32 v38, vcc, s37, v6
	s_nop 1
	v_addc_co_u32_e32 v39, vcc, 0, v7, vcc
	global_load_dword v2, v[6:7], off
	global_load_dword v45, v[8:9], off
	global_load_dword v46, v[12:13], off
	global_load_dword v47, v[14:15], off
	global_load_dword v48, v[16:17], off
	global_load_dword v49, v[18:19], off
	global_load_dword v50, v[20:21], off
	global_load_dword v51, v[22:23], off
	global_load_dword v52, v[24:25], off
	global_load_dword v53, v[26:27], off
	global_load_dword v54, v[28:29], off
	global_load_dword v55, v[30:31], off
	global_load_dword v56, v[32:33], off
	global_load_dword v57, v[34:35], off
	global_load_dword v58, v[36:37], off
	global_load_dword v6, v[38:39], off
	global_load_dword v7, v[4:5], off
	global_load_dword v8, v[10:11], off
	v_mul_u32_u24_sdwa v66, v65, s21 dst_sel:DWORD dst_unused:UNUSED_PAD src0_sel:WORD_0 src1_sel:DWORD
	v_lshrrev_b32_e32 v106, 22, v66
	v_mul_lo_u16_e32 v66, 0x60, v106
	v_mul_u32_u24_e32 v68, 0x300, v106
	v_sub_u16_e32 v107, v65, v66
	v_lshlrev_b32_e32 v66, 2, v68
	v_add_u32_e32 v68, s20, v107
	v_ashrrev_i32_e32 v69, 31, v68
	v_lshlrev_b64 v[68:69], 2, v[68:69]
	s_waitcnt lgkmcnt(0)
	v_lshl_add_u64 v[70:71], s[4:5], 0, v[68:69]
	v_lshl_add_u64 v[72:73], s[6:7], 0, v[68:69]
	v_lshl_add_u64 v[70:71], v[70:71], 0, v[66:67]
	global_load_dword v108, v[72:73], off
	v_add_co_u32_e32 v72, vcc, s22, v70
	v_mul_u32_u24_e32 v76, 0x60000, v106
	s_nop 0
	v_addc_co_u32_e32 v73, vcc, 0, v71, vcc
	v_lshlrev_b32_e32 v66, 2, v76
	v_add_co_u32_e32 v76, vcc, s23, v70
	v_lshl_add_u64 v[104:105], s[16:17], 0, v[66:67]
	s_nop 0
	v_addc_co_u32_e32 v77, vcc, 0, v71, vcc
	v_add_co_u32_e32 v78, vcc, s24, v70
	v_lshl_add_u64 v[74:75], s[12:13], 0, v[68:69]
	s_nop 0
	v_addc_co_u32_e32 v79, vcc, 0, v71, vcc
	v_add_co_u32_e32 v80, vcc, s25, v70
	v_lshl_add_u64 v[68:69], v[104:105], 0, v[68:69]
	s_nop 0
	v_addc_co_u32_e32 v81, vcc, 0, v71, vcc
	v_add_co_u32_e32 v82, vcc, s26, v70
	s_nop 1
	v_addc_co_u32_e32 v83, vcc, 0, v71, vcc
	v_add_co_u32_e32 v84, vcc, s27, v70
	s_nop 1
	v_addc_co_u32_e32 v85, vcc, 0, v71, vcc
	v_add_co_u32_e32 v86, vcc, s28, v70
	s_nop 1
	v_addc_co_u32_e32 v87, vcc, 0, v71, vcc
	v_add_co_u32_e32 v88, vcc, s29, v70
	s_nop 1
	v_addc_co_u32_e32 v89, vcc, 0, v71, vcc
	v_add_co_u32_e32 v90, vcc, s30, v70
	s_nop 1
	v_addc_co_u32_e32 v91, vcc, 0, v71, vcc
	v_add_co_u32_e32 v92, vcc, s31, v70
	s_nop 1
	v_addc_co_u32_e32 v93, vcc, 0, v71, vcc
	v_add_co_u32_e32 v94, vcc, s33, v70
	s_nop 1
	v_addc_co_u32_e32 v95, vcc, 0, v71, vcc
	v_add_co_u32_e32 v96, vcc, s34, v70
	s_nop 1
	v_addc_co_u32_e32 v97, vcc, 0, v71, vcc
	v_add_co_u32_e32 v98, vcc, s35, v70
	s_nop 1
	v_addc_co_u32_e32 v99, vcc, 0, v71, vcc
	v_add_co_u32_e32 v100, vcc, s36, v70
	s_nop 1
	v_addc_co_u32_e32 v101, vcc, 0, v71, vcc
	v_add_co_u32_e32 v102, vcc, s37, v70
	s_nop 1
	v_addc_co_u32_e32 v103, vcc, 0, v71, vcc
	global_load_dword v66, v[70:71], off
	global_load_dword v109, v[72:73], off
	global_load_dword v110, v[76:77], off
	global_load_dword v111, v[78:79], off
	global_load_dword v112, v[80:81], off
	global_load_dword v113, v[82:83], off
	global_load_dword v114, v[84:85], off
	global_load_dword v115, v[86:87], off
	global_load_dword v116, v[88:89], off
	global_load_dword v117, v[90:91], off
	global_load_dword v118, v[92:93], off
	global_load_dword v119, v[94:95], off
	global_load_dword v120, v[96:97], off
	global_load_dword v121, v[98:99], off
	global_load_dword v122, v[100:101], off
	global_load_dword v70, v[102:103], off
	global_load_dword v71, v[68:69], off
	global_load_dword v72, v[74:75], off
	v_mul_u32_u24_sdwa v130, v129, s21 dst_sel:DWORD dst_unused:UNUSED_PAD src0_sel:WORD_0 src1_sel:DWORD
	v_lshrrev_b32_e32 v170, 22, v130
	v_mul_lo_u16_e32 v130, 0x60, v170
	v_mul_u32_u24_e32 v132, 0x300, v170
	v_sub_u16_e32 v171, v129, v130
	v_lshlrev_b32_e32 v130, 2, v132
	v_add_u32_e32 v132, s20, v171
	v_ashrrev_i32_e32 v133, 31, v132
	v_lshlrev_b64 v[132:133], 2, v[132:133]
	s_waitcnt lgkmcnt(0)
	v_lshl_add_u64 v[134:135], s[4:5], 0, v[132:133]
	v_lshl_add_u64 v[136:137], s[6:7], 0, v[132:133]
	v_lshl_add_u64 v[134:135], v[134:135], 0, v[130:131]
	global_load_dword v172, v[136:137], off
	v_add_co_u32_e32 v136, vcc, s22, v134
	v_mul_u32_u24_e32 v140, 0x60000, v170
	s_nop 0
	v_addc_co_u32_e32 v137, vcc, 0, v135, vcc
	v_lshlrev_b32_e32 v130, 2, v140
	v_add_co_u32_e32 v140, vcc, s23, v134
	v_lshl_add_u64 v[168:169], s[16:17], 0, v[130:131]
	s_nop 0
	v_addc_co_u32_e32 v141, vcc, 0, v135, vcc
	v_add_co_u32_e32 v142, vcc, s24, v134
	v_lshl_add_u64 v[138:139], s[12:13], 0, v[132:133]
	s_nop 0
	v_addc_co_u32_e32 v143, vcc, 0, v135, vcc
	v_add_co_u32_e32 v144, vcc, s25, v134
	v_lshl_add_u64 v[132:133], v[168:169], 0, v[132:133]
	s_nop 0
	v_addc_co_u32_e32 v145, vcc, 0, v135, vcc
	v_add_co_u32_e32 v146, vcc, s26, v134
	s_nop 1
	v_addc_co_u32_e32 v147, vcc, 0, v135, vcc
	v_add_co_u32_e32 v148, vcc, s27, v134
	s_nop 1
	v_addc_co_u32_e32 v149, vcc, 0, v135, vcc
	v_add_co_u32_e32 v150, vcc, s28, v134
	s_nop 1
	v_addc_co_u32_e32 v151, vcc, 0, v135, vcc
	v_add_co_u32_e32 v152, vcc, s29, v134
	s_nop 1
	v_addc_co_u32_e32 v153, vcc, 0, v135, vcc
	v_add_co_u32_e32 v154, vcc, s30, v134
	s_nop 1
	v_addc_co_u32_e32 v155, vcc, 0, v135, vcc
	v_add_co_u32_e32 v156, vcc, s31, v134
	s_nop 1
	v_addc_co_u32_e32 v157, vcc, 0, v135, vcc
	v_add_co_u32_e32 v158, vcc, s33, v134
	s_nop 1
	v_addc_co_u32_e32 v159, vcc, 0, v135, vcc
	v_add_co_u32_e32 v160, vcc, s34, v134
	s_nop 1
	v_addc_co_u32_e32 v161, vcc, 0, v135, vcc
	v_add_co_u32_e32 v162, vcc, s35, v134
	s_nop 1
	v_addc_co_u32_e32 v163, vcc, 0, v135, vcc
	v_add_co_u32_e32 v164, vcc, s36, v134
	s_nop 1
	v_addc_co_u32_e32 v165, vcc, 0, v135, vcc
	v_add_co_u32_e32 v166, vcc, s37, v134
	s_nop 1
	v_addc_co_u32_e32 v167, vcc, 0, v135, vcc
	global_load_dword v130, v[134:135], off
	global_load_dword v173, v[136:137], off
	global_load_dword v174, v[140:141], off
	global_load_dword v175, v[142:143], off
	global_load_dword v176, v[144:145], off
	global_load_dword v177, v[146:147], off
	global_load_dword v178, v[148:149], off
	global_load_dword v179, v[150:151], off
	global_load_dword v180, v[152:153], off
	global_load_dword v181, v[154:155], off
	global_load_dword v182, v[156:157], off
	global_load_dword v183, v[158:159], off
	global_load_dword v184, v[160:161], off
	global_load_dword v185, v[162:163], off
	global_load_dword v186, v[164:165], off
	global_load_dword v134, v[166:167], off
	global_load_dword v135, v[132:133], off
	global_load_dword v136, v[138:139], off
	s_lshl_b32 s40, s2, 6
	s_mul_i32 s44, s3, 0x48000
	s_ashr_i32 s41, s40, 31
	s_mul_hi_i32 s45, s20, 0xc00
	s_add_u32 s44, s8, s44
	s_addc_u32 s45, s9, s45
	s_lshl_b64 s[40:41], s[40:41], 2
	s_add_u32 s44, s44, s40
	v_lshlrev_b32_e32 v194, 4, v0
	v_lshrrev_b32_e32 v193, 4, v0
	s_addc_u32 s45, s45, s41
	v_and_b32_e32 v218, 0xf0, v194
	v_mov_b32_e32 v219, 0
	v_lshl_add_u64 v[214:215], s[44:45], 0, v[218:219]
	v_mul_u32_u24_e32 v194, 0xc00, v193
	v_mov_b32_e32 v195, v219
	s_movk_i32 s42, 0xc00
	v_lshl_add_u64 v[196:197], v[214:215], 0, v[194:195]
	v_mov_b32_e32 v195, 0xc000
	v_mad_u32_u24 v198, v193, s42, v195
	v_mov_b32_e32 v195, 0x18000
	v_mad_u32_u24 v200, v193, s42, v195
	v_mov_b32_e32 v201, v219
	v_mov_b32_e32 v195, 0x24000
	v_mov_b32_e32 v199, v219
	v_lshl_add_u64 v[202:203], v[214:215], 0, v[200:201]
	v_mad_u32_u24 v200, v193, s42, v195
	v_lshl_add_u64 v[198:199], v[214:215], 0, v[198:199]
	v_lshl_add_u64 v[206:207], v[214:215], 0, v[200:201]
	v_or_b32_e32 v200, 0x30000, v194
	global_load_dwordx4 v[194:197], v[196:197], off
	v_lshl_add_u64 v[210:211], v[214:215], 0, v[200:201]
	global_load_dwordx4 v[198:201], v[198:199], off
	v_mov_b32_e32 v208, 0x3c000
	global_load_dwordx4 v[202:205], v[202:203], off
	v_mad_u32_u24 v216, v193, s42, v208
	global_load_dwordx4 v[206:209], v[206:207], off
	v_mov_b32_e32 v217, v219
	global_load_dwordx4 v[210:213], v[210:211], off
	v_lshl_add_u64 v[214:215], v[214:215], 0, v[216:217]
	global_load_dwordx4 v[214:217], v[214:215], off
	v_lshlrev_b32_e32 v4, 2, v43
	v_mad_u32_u24 v4, v42, s38, v4
	s_waitcnt vmcnt(61)
	v_add_f32_e32 v2, 0, v2
	s_waitcnt vmcnt(60)
	v_add_f32_e32 v2, v2, v45
	s_waitcnt vmcnt(59)
	v_add_f32_e32 v2, v2, v46
	s_waitcnt vmcnt(58)
	v_add_f32_e32 v2, v2, v47
	s_waitcnt vmcnt(57)
	v_add_f32_e32 v2, v2, v48
	s_waitcnt vmcnt(56)
	v_add_f32_e32 v2, v2, v49
	s_waitcnt vmcnt(55)
	v_add_f32_e32 v2, v2, v50
	s_waitcnt vmcnt(54)
	v_add_f32_e32 v2, v2, v51
	s_waitcnt vmcnt(53)
	v_add_f32_e32 v2, v2, v52
	s_waitcnt vmcnt(52)
	v_add_f32_e32 v2, v2, v53
	s_waitcnt vmcnt(51)
	v_add_f32_e32 v2, v2, v54
	s_waitcnt vmcnt(50)
	v_add_f32_e32 v2, v2, v55
	s_waitcnt vmcnt(49)
	v_add_f32_e32 v2, v2, v56
	s_waitcnt vmcnt(48)
	v_add_f32_e32 v2, v2, v57
	s_waitcnt vmcnt(47)
	v_add_f32_e32 v2, v2, v58
	s_waitcnt vmcnt(46)
	v_add_f32_e32 v2, v2, v6
	v_add_f32_e32 v2, v2, v44
	s_waitcnt vmcnt(45)
	v_add_f32_e32 v2, v2, v7
	s_waitcnt vmcnt(44)
	v_mul_f32_e32 v5, v2, v8
	ds_write2st64_b32 v4, v5, v2 offset0:160 offset1:175
	v_lshlrev_b32_e32 v68, 2, v107
	v_mad_u32_u24 v68, v106, s38, v68
	s_waitcnt vmcnt(42)
	v_add_f32_e32 v66, 0, v66
	s_waitcnt vmcnt(41)
	v_add_f32_e32 v66, v66, v109
	s_waitcnt vmcnt(40)
	v_add_f32_e32 v66, v66, v110
	s_waitcnt vmcnt(39)
	v_add_f32_e32 v66, v66, v111
	s_waitcnt vmcnt(38)
	v_add_f32_e32 v66, v66, v112
	s_waitcnt vmcnt(37)
	v_add_f32_e32 v66, v66, v113
	s_waitcnt vmcnt(36)
	v_add_f32_e32 v66, v66, v114
	s_waitcnt vmcnt(35)
	v_add_f32_e32 v66, v66, v115
	s_waitcnt vmcnt(34)
	v_add_f32_e32 v66, v66, v116
	s_waitcnt vmcnt(33)
	v_add_f32_e32 v66, v66, v117
	s_waitcnt vmcnt(32)
	v_add_f32_e32 v66, v66, v118
	s_waitcnt vmcnt(31)
	v_add_f32_e32 v66, v66, v119
	s_waitcnt vmcnt(30)
	v_add_f32_e32 v66, v66, v120
	s_waitcnt vmcnt(29)
	v_add_f32_e32 v66, v66, v121
	s_waitcnt vmcnt(28)
	v_add_f32_e32 v66, v66, v122
	s_waitcnt vmcnt(27)
	v_add_f32_e32 v66, v66, v70
	v_add_f32_e32 v66, v66, v108
	s_waitcnt vmcnt(26)
	v_add_f32_e32 v66, v66, v71
	s_waitcnt vmcnt(25)
	v_mul_f32_e32 v69, v66, v72
	ds_write2st64_b32 v68, v69, v66 offset0:160 offset1:175
	v_lshlrev_b32_e32 v132, 2, v171
	v_mad_u32_u24 v132, v170, s38, v132
	s_waitcnt vmcnt(23)
	v_add_f32_e32 v130, 0, v130
	s_waitcnt vmcnt(22)
	v_add_f32_e32 v130, v130, v173
	s_waitcnt vmcnt(21)
	v_add_f32_e32 v130, v130, v174
	s_waitcnt vmcnt(20)
	v_add_f32_e32 v130, v130, v175
	s_waitcnt vmcnt(19)
	v_add_f32_e32 v130, v130, v176
	s_waitcnt vmcnt(18)
	v_add_f32_e32 v130, v130, v177
	s_waitcnt vmcnt(17)
	v_add_f32_e32 v130, v130, v178
	s_waitcnt vmcnt(16)
	v_add_f32_e32 v130, v130, v179
	s_waitcnt vmcnt(15)
	v_add_f32_e32 v130, v130, v180
	s_waitcnt vmcnt(14)
	v_add_f32_e32 v130, v130, v181
	s_waitcnt vmcnt(13)
	v_add_f32_e32 v130, v130, v182
	s_waitcnt vmcnt(12)
	v_add_f32_e32 v130, v130, v183
	s_waitcnt vmcnt(11)
	v_add_f32_e32 v130, v130, v184
	s_waitcnt vmcnt(10)
	v_add_f32_e32 v130, v130, v185
	s_waitcnt vmcnt(9)
	v_add_f32_e32 v130, v130, v186
	s_waitcnt vmcnt(8)
	v_add_f32_e32 v130, v130, v134
	v_add_f32_e32 v130, v130, v172
	s_waitcnt vmcnt(7)
	v_add_f32_e32 v130, v130, v135
	s_waitcnt vmcnt(6)
	v_mul_f32_e32 v133, v130, v136
	ds_write2st64_b32 v132, v133, v130 offset0:160 offset1:175

.LBB8_7:
	s_or_b64 exec, exec, s[0:1]
	s_waitcnt vmcnt(0)
	s_lshl_b32 s0, s2, 6
	s_mul_i32 s6, s3, 0x48000
	s_ashr_i32 s1, s0, 31
	s_mul_hi_i32 s7, s20, 0xc00
	s_add_u32 s6, s8, s6
	s_addc_u32 s7, s9, s7
	s_lshl_b64 s[0:1], s[0:1], 2
	s_add_u32 s6, s6, s0
	v_lshlrev_b32_e32 v2, 4, v0
	v_lshrrev_b32_e32 v1, 4, v0
	s_addc_u32 s7, s7, s1
	v_and_b32_e32 v26, 0xf0, v2
	v_mov_b32_e32 v27, 0
	v_lshl_add_u64 v[22:23], s[6:7], 0, v[26:27]
	v_mul_u32_u24_e32 v2, 0xc00, v1
	v_mov_b32_e32 v3, v27
	s_movk_i32 s2, 0xc00
	v_lshl_add_u64 v[4:5], v[22:23], 0, v[2:3]
	v_mov_b32_e32 v3, 0xc000
	v_mad_u32_u24 v6, v1, s2, v3
	v_mov_b32_e32 v3, 0x18000
	v_mad_u32_u24 v8, v1, s2, v3
	v_mov_b32_e32 v9, v27
	v_mov_b32_e32 v3, 0x24000
	v_mov_b32_e32 v7, v27
	v_lshl_add_u64 v[10:11], v[22:23], 0, v[8:9]
	v_mad_u32_u24 v8, v1, s2, v3
	v_lshl_add_u64 v[6:7], v[22:23], 0, v[6:7]
	v_lshl_add_u64 v[14:15], v[22:23], 0, v[8:9]
	v_or_b32_e32 v8, 0x30000, v2
	v_mov_b32_e32 v2, v194
	v_mov_b32_e32 v3, v195
	v_mov_b32_e32 v4, v196
	v_mov_b32_e32 v5, v197
	v_lshl_add_u64 v[18:19], v[22:23], 0, v[8:9]
	v_mov_b32_e32 v6, v198
	v_mov_b32_e32 v7, v199
	v_mov_b32_e32 v8, v200
	v_mov_b32_e32 v9, v201
	v_mov_b32_e32 v16, 0x3c000
	v_mov_b32_e32 v10, v202
	v_mov_b32_e32 v11, v203
	v_mov_b32_e32 v12, v204
	v_mov_b32_e32 v13, v205
	v_mad_u32_u24 v24, v1, s2, v16
	v_mov_b32_e32 v14, v206
	v_mov_b32_e32 v15, v207
	v_mov_b32_e32 v16, v208
	v_mov_b32_e32 v17, v209
	v_mov_b32_e32 v25, v27
	v_mov_b32_e32 v18, v210
	v_mov_b32_e32 v19, v211
	v_mov_b32_e32 v20, v212
	v_mov_b32_e32 v21, v213
	v_lshl_add_u64 v[22:23], v[22:23], 0, v[24:25]
	v_mov_b32_e32 v22, v214
	v_mov_b32_e32 v23, v215
	v_mov_b32_e32 v24, v216
	v_mov_b32_e32 v25, v217
	v_lshlrev_b32_e32 v28, 2, v1
	v_add_u32_e32 v70, 0xa000, v28
	v_add_u32_e32 v76, 0xa400, v28
	v_add_u32_e32 v82, 0xa800, v28
	v_add_u32_e32 v86, 0xac00, v28
	v_mul_u32_u24_e32 v1, 0xa00, v1
	ds_read2_b32 v[28:29], v70 offset1:16
	ds_read2_b32 v[32:33], v70 offset0:96 offset1:112
	ds_read2_b32 v[34:35], v70 offset0:192 offset1:208
	ds_read2_b32 v[36:37], v76 offset0:32 offset1:48
	ds_read2_b32 v[38:39], v76 offset0:128 offset1:144
	ds_read2_b32 v[40:41], v76 offset0:224 offset1:240
	ds_read2_b32 v[42:43], v82 offset0:64 offset1:80
	ds_read2_b32 v[44:45], v82 offset0:160 offset1:176
	ds_read2_b32 v[46:47], v86 offset1:16
	ds_read2_b32 v[48:49], v86 offset0:96 offset1:112
	ds_read2_b32 v[30:31], v70 offset0:32 offset1:48
	ds_read2_b32 v[50:51], v70 offset0:128 offset1:144
	ds_read2_b32 v[52:53], v70 offset0:224 offset1:240
	ds_read2_b32 v[54:55], v76 offset0:64 offset1:80
	ds_read2_b32 v[56:57], v76 offset0:160 offset1:176
	ds_read2_b32 v[58:59], v82 offset1:16
	ds_read2_b32 v[60:61], v82 offset0:96 offset1:112
	ds_read2_b32 v[62:63], v82 offset0:192 offset1:208
	ds_read2_b32 v[64:65], v86 offset0:32 offset1:48
	ds_read2_b32 v[66:67], v86 offset0:128 offset1:144
	ds_read2_b32 v[68:69], v70 offset0:64 offset1:80
	ds_read2_b32 v[70:71], v70 offset0:160 offset1:176
	ds_read2_b32 v[72:73], v76 offset1:16
	ds_read2_b32 v[74:75], v76 offset0:96 offset1:112
	ds_read2_b32 v[76:77], v76 offset0:192 offset1:208
	ds_read2_b32 v[78:79], v82 offset0:32 offset1:48
	ds_read2_b32 v[80:81], v82 offset0:128 offset1:144
	ds_read2_b32 v[82:83], v82 offset0:224 offset1:240
	ds_read2_b32 v[84:85], v86 offset0:64 offset1:80
	ds_read2_b32 v[86:87], v86 offset0:160 offset1:176
	v_or_b32_e32 v1, v1, v26
	s_waitcnt lgkmcnt(14)
	v_mov_b32_e32 v26, v29
	v_mov_b32_e32 v88, v31
	s_waitcnt lgkmcnt(9)
	v_mov_b32_e32 v90, v69
	s_movk_i32 s6, 0x280
	v_cmp_gt_u32_e32 vcc, s6, v0
	s_waitcnt vmcnt(5)
	v_pk_fma_f32 v[92:93], v[2:3], v[28:29], 0 op_sel_hi:[1,0,0]
	v_pk_fma_f32 v[28:29], v[4:5], v[28:29], 0 op_sel_hi:[1,0,0]
	s_waitcnt vmcnt(4)
	v_pk_fma_f32 v[92:93], v[6:7], v[26:27], v[92:93] op_sel_hi:[1,0,1]
	v_pk_fma_f32 v[28:29], v[8:9], v[26:27], v[28:29] op_sel_hi:[1,0,1]
	s_waitcnt vmcnt(3)
	v_pk_fma_f32 v[92:93], v[10:11], v[30:31], v[92:93] op_sel_hi:[1,0,1]
	v_pk_fma_f32 v[28:29], v[12:13], v[30:31], v[28:29] op_sel_hi:[1,0,1]
	s_waitcnt vmcnt(2)
	v_pk_fma_f32 v[30:31], v[14:15], v[88:89], v[92:93] op_sel_hi:[1,0,1]
	v_pk_fma_f32 v[28:29], v[16:17], v[88:89], v[28:29] op_sel_hi:[1,0,1]
	s_waitcnt vmcnt(1)
	v_pk_fma_f32 v[30:31], v[18:19], v[68:69], v[30:31] op_sel_hi:[1,0,1]
	v_pk_fma_f32 v[68:69], v[20:21], v[68:69], v[28:29] op_sel_hi:[1,0,1]
	s_waitcnt vmcnt(0)
	v_pk_fma_f32 v[28:29], v[22:23], v[90:91], v[30:31] op_sel_hi:[1,0,1]
	v_pk_fma_f32 v[30:31], v[24:25], v[90:91], v[68:69] op_sel_hi:[1,0,1]
	ds_write_b128 v1, v[28:31]
	v_pk_fma_f32 v[28:29], v[2:3], v[32:33], 0 op_sel_hi:[1,0,0]
	v_mov_b32_e32 v26, v33
	v_pk_fma_f32 v[32:33], v[4:5], v[32:33], 0 op_sel_hi:[1,0,0]
	v_pk_fma_f32 v[28:29], v[6:7], v[26:27], v[28:29] op_sel_hi:[1,0,1]
	v_pk_fma_f32 v[32:33], v[8:9], v[26:27], v[32:33] op_sel_hi:[1,0,1]
	v_pk_fma_f32 v[28:29], v[10:11], v[50:51], v[28:29] op_sel_hi:[1,0,1]
	v_mov_b32_e32 v30, v51
	v_pk_fma_f32 v[32:33], v[12:13], v[50:51], v[32:33] op_sel_hi:[1,0,1]
	v_pk_fma_f32 v[28:29], v[14:15], v[30:31], v[28:29] op_sel_hi:[1,0,1]
	v_pk_fma_f32 v[30:31], v[16:17], v[30:31], v[32:33] op_sel_hi:[1,0,1]
	s_waitcnt lgkmcnt(9)
	v_pk_fma_f32 v[28:29], v[18:19], v[70:71], v[28:29] op_sel_hi:[1,0,1]
	v_mov_b32_e32 v68, v71
	v_pk_fma_f32 v[30:31], v[20:21], v[70:71], v[30:31] op_sel_hi:[1,0,1]
	v_pk_fma_f32 v[28:29], v[22:23], v[68:69], v[28:29] op_sel_hi:[1,0,1]
	v_pk_fma_f32 v[30:31], v[24:25], v[68:69], v[30:31] op_sel_hi:[1,0,1]
	ds_write_b128 v1, v[28:31] offset:256
	v_pk_fma_f32 v[28:29], v[2:3], v[34:35], 0 op_sel_hi:[1,0,0]
	v_mov_b32_e32 v26, v35
	v_pk_fma_f32 v[34:35], v[4:5], v[34:35], 0 op_sel_hi:[1,0,0]
	v_pk_fma_f32 v[28:29], v[6:7], v[26:27], v[28:29] op_sel_hi:[1,0,1]
	v_pk_fma_f32 v[34:35], v[8:9], v[26:27], v[34:35] op_sel_hi:[1,0,1]
	v_pk_fma_f32 v[28:29], v[10:11], v[52:53], v[28:29] op_sel_hi:[1,0,1]
	v_mov_b32_e32 v30, v53
	v_pk_fma_f32 v[34:35], v[12:13], v[52:53], v[34:35] op_sel_hi:[1,0,1]
	v_pk_fma_f32 v[28:29], v[14:15], v[30:31], v[28:29] op_sel_hi:[1,0,1]
	v_pk_fma_f32 v[30:31], v[16:17], v[30:31], v[34:35] op_sel_hi:[1,0,1]
	s_waitcnt lgkmcnt(9)
	v_pk_fma_f32 v[28:29], v[18:19], v[72:73], v[28:29] op_sel_hi:[1,0,1]
	v_mov_b32_e32 v32, v73
	v_pk_fma_f32 v[30:31], v[20:21], v[72:73], v[30:31] op_sel_hi:[1,0,1]
	v_pk_fma_f32 v[28:29], v[22:23], v[32:33], v[28:29] op_sel_hi:[1,0,1]
	v_pk_fma_f32 v[30:31], v[24:25], v[32:33], v[30:31] op_sel_hi:[1,0,1]
	ds_write_b128 v1, v[28:31] offset:512
	v_pk_fma_f32 v[28:29], v[2:3], v[36:37], 0 op_sel_hi:[1,0,0]
	v_mov_b32_e32 v26, v37
	v_pk_fma_f32 v[34:35], v[4:5], v[36:37], 0 op_sel_hi:[1,0,0]
	v_pk_fma_f32 v[28:29], v[6:7], v[26:27], v[28:29] op_sel_hi:[1,0,1]
	v_pk_fma_f32 v[34:35], v[8:9], v[26:27], v[34:35] op_sel_hi:[1,0,1]
	v_pk_fma_f32 v[28:29], v[10:11], v[54:55], v[28:29] op_sel_hi:[1,0,1]
	v_mov_b32_e32 v30, v55
	v_pk_fma_f32 v[34:35], v[12:13], v[54:55], v[34:35] op_sel_hi:[1,0,1]
	v_pk_fma_f32 v[28:29], v[14:15], v[30:31], v[28:29] op_sel_hi:[1,0,1]
	v_pk_fma_f32 v[30:31], v[16:17], v[30:31], v[34:35] op_sel_hi:[1,0,1]
	s_waitcnt lgkmcnt(9)
	v_pk_fma_f32 v[28:29], v[18:19], v[74:75], v[28:29] op_sel_hi:[1,0,1]
	v_mov_b32_e32 v32, v75
	v_pk_fma_f32 v[30:31], v[20:21], v[74:75], v[30:31] op_sel_hi:[1,0,1]
	v_pk_fma_f32 v[28:29], v[22:23], v[32:33], v[28:29] op_sel_hi:[1,0,1]
	v_pk_fma_f32 v[30:31], v[24:25], v[32:33], v[30:31] op_sel_hi:[1,0,1]
	ds_write_b128 v1, v[28:31] offset:768
	v_pk_fma_f32 v[28:29], v[2:3], v[38:39], 0 op_sel_hi:[1,0,0]
	v_mov_b32_e32 v26, v39
	v_pk_fma_f32 v[34:35], v[4:5], v[38:39], 0 op_sel_hi:[1,0,0]
	v_pk_fma_f32 v[28:29], v[6:7], v[26:27], v[28:29] op_sel_hi:[1,0,1]
	v_pk_fma_f32 v[34:35], v[8:9], v[26:27], v[34:35] op_sel_hi:[1,0,1]
	v_pk_fma_f32 v[28:29], v[10:11], v[56:57], v[28:29] op_sel_hi:[1,0,1]
	v_mov_b32_e32 v30, v57
	v_pk_fma_f32 v[34:35], v[12:13], v[56:57], v[34:35] op_sel_hi:[1,0,1]
	v_pk_fma_f32 v[28:29], v[14:15], v[30:31], v[28:29] op_sel_hi:[1,0,1]
	v_pk_fma_f32 v[30:31], v[16:17], v[30:31], v[34:35] op_sel_hi:[1,0,1]
	s_waitcnt lgkmcnt(9)
	v_pk_fma_f32 v[28:29], v[18:19], v[76:77], v[28:29] op_sel_hi:[1,0,1]
	v_mov_b32_e32 v32, v77
	v_pk_fma_f32 v[30:31], v[20:21], v[76:77], v[30:31] op_sel_hi:[1,0,1]
	v_pk_fma_f32 v[28:29], v[22:23], v[32:33], v[28:29] op_sel_hi:[1,0,1]
	v_pk_fma_f32 v[30:31], v[24:25], v[32:33], v[30:31] op_sel_hi:[1,0,1]
	ds_write_b128 v1, v[28:31] offset:1024
	v_pk_fma_f32 v[28:29], v[2:3], v[40:41], 0 op_sel_hi:[1,0,0]
	v_mov_b32_e32 v26, v41
	v_pk_fma_f32 v[34:35], v[4:5], v[40:41], 0 op_sel_hi:[1,0,0]
	v_pk_fma_f32 v[28:29], v[6:7], v[26:27], v[28:29] op_sel_hi:[1,0,1]
	v_pk_fma_f32 v[34:35], v[8:9], v[26:27], v[34:35] op_sel_hi:[1,0,1]
	v_pk_fma_f32 v[28:29], v[10:11], v[58:59], v[28:29] op_sel_hi:[1,0,1]
	v_mov_b32_e32 v30, v59
	v_pk_fma_f32 v[34:35], v[12:13], v[58:59], v[34:35] op_sel_hi:[1,0,1]
	v_pk_fma_f32 v[28:29], v[14:15], v[30:31], v[28:29] op_sel_hi:[1,0,1]
	v_pk_fma_f32 v[30:31], v[16:17], v[30:31], v[34:35] op_sel_hi:[1,0,1]
	s_waitcnt lgkmcnt(9)
	v_pk_fma_f32 v[28:29], v[18:19], v[78:79], v[28:29] op_sel_hi:[1,0,1]
	v_mov_b32_e32 v32, v79
	v_pk_fma_f32 v[30:31], v[20:21], v[78:79], v[30:31] op_sel_hi:[1,0,1]
	v_pk_fma_f32 v[28:29], v[22:23], v[32:33], v[28:29] op_sel_hi:[1,0,1]
	v_pk_fma_f32 v[30:31], v[24:25], v[32:33], v[30:31] op_sel_hi:[1,0,1]
	ds_write_b128 v1, v[28:31] offset:1280
	v_pk_fma_f32 v[28:29], v[2:3], v[42:43], 0 op_sel_hi:[1,0,0]
	v_mov_b32_e32 v26, v43
	v_pk_fma_f32 v[34:35], v[4:5], v[42:43], 0 op_sel_hi:[1,0,0]
	v_pk_fma_f32 v[28:29], v[6:7], v[26:27], v[28:29] op_sel_hi:[1,0,1]
	v_pk_fma_f32 v[34:35], v[8:9], v[26:27], v[34:35] op_sel_hi:[1,0,1]
	v_pk_fma_f32 v[28:29], v[10:11], v[60:61], v[28:29] op_sel_hi:[1,0,1]
	v_mov_b32_e32 v30, v61
	v_pk_fma_f32 v[34:35], v[12:13], v[60:61], v[34:35] op_sel_hi:[1,0,1]
	v_pk_fma_f32 v[28:29], v[14:15], v[30:31], v[28:29] op_sel_hi:[1,0,1]
	v_pk_fma_f32 v[30:31], v[16:17], v[30:31], v[34:35] op_sel_hi:[1,0,1]
	s_waitcnt lgkmcnt(9)
	v_pk_fma_f32 v[28:29], v[18:19], v[80:81], v[28:29] op_sel_hi:[1,0,1]
	v_mov_b32_e32 v32, v81
	v_pk_fma_f32 v[30:31], v[20:21], v[80:81], v[30:31] op_sel_hi:[1,0,1]
	v_pk_fma_f32 v[28:29], v[22:23], v[32:33], v[28:29] op_sel_hi:[1,0,1]
	v_pk_fma_f32 v[30:31], v[24:25], v[32:33], v[30:31] op_sel_hi:[1,0,1]
	ds_write_b128 v1, v[28:31] offset:1536
	v_pk_fma_f32 v[28:29], v[2:3], v[44:45], 0 op_sel_hi:[1,0,0]
	v_mov_b32_e32 v26, v45
	v_pk_fma_f32 v[34:35], v[4:5], v[44:45], 0 op_sel_hi:[1,0,0]
	v_pk_fma_f32 v[28:29], v[6:7], v[26:27], v[28:29] op_sel_hi:[1,0,1]
	v_pk_fma_f32 v[34:35], v[8:9], v[26:27], v[34:35] op_sel_hi:[1,0,1]
	v_pk_fma_f32 v[28:29], v[10:11], v[62:63], v[28:29] op_sel_hi:[1,0,1]
	v_mov_b32_e32 v30, v63
	v_pk_fma_f32 v[34:35], v[12:13], v[62:63], v[34:35] op_sel_hi:[1,0,1]
	v_pk_fma_f32 v[28:29], v[14:15], v[30:31], v[28:29] op_sel_hi:[1,0,1]
	v_pk_fma_f32 v[30:31], v[16:17], v[30:31], v[34:35] op_sel_hi:[1,0,1]
	s_waitcnt lgkmcnt(9)
	v_pk_fma_f32 v[28:29], v[18:19], v[82:83], v[28:29] op_sel_hi:[1,0,1]
	v_mov_b32_e32 v32, v83
	v_pk_fma_f32 v[30:31], v[20:21], v[82:83], v[30:31] op_sel_hi:[1,0,1]
	v_pk_fma_f32 v[28:29], v[22:23], v[32:33], v[28:29] op_sel_hi:[1,0,1]
	v_pk_fma_f32 v[30:31], v[24:25], v[32:33], v[30:31] op_sel_hi:[1,0,1]
	ds_write_b128 v1, v[28:31] offset:1792
	v_pk_fma_f32 v[28:29], v[2:3], v[46:47], 0 op_sel_hi:[1,0,0]
	v_mov_b32_e32 v26, v47
	v_pk_fma_f32 v[34:35], v[4:5], v[46:47], 0 op_sel_hi:[1,0,0]
	v_pk_fma_f32 v[28:29], v[6:7], v[26:27], v[28:29] op_sel_hi:[1,0,1]
	v_pk_fma_f32 v[34:35], v[8:9], v[26:27], v[34:35] op_sel_hi:[1,0,1]
	v_pk_fma_f32 v[2:3], v[2:3], v[48:49], 0 op_sel_hi:[1,0,0]
	v_mov_b32_e32 v26, v49
	v_pk_fma_f32 v[4:5], v[4:5], v[48:49], 0 op_sel_hi:[1,0,0]
	v_pk_fma_f32 v[2:3], v[6:7], v[26:27], v[2:3] op_sel_hi:[1,0,1]
	v_pk_fma_f32 v[4:5], v[8:9], v[26:27], v[4:5] op_sel_hi:[1,0,1]
	v_pk_fma_f32 v[28:29], v[10:11], v[64:65], v[28:29] op_sel_hi:[1,0,1]
	v_mov_b32_e32 v30, v65
	v_pk_fma_f32 v[34:35], v[12:13], v[64:65], v[34:35] op_sel_hi:[1,0,1]
	v_pk_fma_f32 v[2:3], v[10:11], v[66:67], v[2:3] op_sel_hi:[1,0,1]
	v_mov_b32_e32 v6, v67
	v_pk_fma_f32 v[4:5], v[12:13], v[66:67], v[4:5] op_sel_hi:[1,0,1]
	v_pk_fma_f32 v[28:29], v[14:15], v[30:31], v[28:29] op_sel_hi:[1,0,1]
	v_pk_fma_f32 v[30:31], v[16:17], v[30:31], v[34:35] op_sel_hi:[1,0,1]
	v_pk_fma_f32 v[2:3], v[14:15], v[6:7], v[2:3] op_sel_hi:[1,0,1]
	v_pk_fma_f32 v[4:5], v[16:17], v[6:7], v[4:5] op_sel_hi:[1,0,1]
	s_waitcnt lgkmcnt(9)
	v_pk_fma_f32 v[28:29], v[18:19], v[84:85], v[28:29] op_sel_hi:[1,0,1]
	v_mov_b32_e32 v32, v85
	v_pk_fma_f32 v[30:31], v[20:21], v[84:85], v[30:31] op_sel_hi:[1,0,1]
	s_waitcnt lgkmcnt(8)
	v_pk_fma_f32 v[2:3], v[18:19], v[86:87], v[2:3] op_sel_hi:[1,0,1]
	v_mov_b32_e32 v10, v87
	v_pk_fma_f32 v[4:5], v[20:21], v[86:87], v[4:5] op_sel_hi:[1,0,1]
	v_pk_fma_f32 v[28:29], v[22:23], v[32:33], v[28:29] op_sel_hi:[1,0,1]
	v_pk_fma_f32 v[30:31], v[24:25], v[32:33], v[30:31] op_sel_hi:[1,0,1]
	v_pk_fma_f32 v[2:3], v[22:23], v[10:11], v[2:3] op_sel_hi:[1,0,1]
	v_pk_fma_f32 v[4:5], v[24:25], v[10:11], v[4:5] op_sel_hi:[1,0,1]
	ds_write_b128 v1, v[28:31] offset:2048
	ds_write_b128 v1, v[2:5] offset:2304
	s_waitcnt lgkmcnt(0)
	s_barrier
	s_and_saveexec_b64 s[6:7], vcc
	s_cbranch_execz .LBB8_10
	s_mul_hi_i32 s6, s3, 0x7800
	s_mulk_i32 s3, 0x7800
	s_add_u32 s0, s0, s3
	v_and_b32_e32 v1, 63, v0
	s_addc_u32 s1, s1, s6
	v_or_b32_e32 v2, 0xffffff00, v0
	v_lshrrev_b32_e32 v4, 6, v0
	v_lshlrev_b32_e32 v26, 2, v1
	v_mov_b64_e32 v[0:1], s[0:1]
	v_mad_u64_u32 v[0:1], s[0:1], v4, s2, v[0:1]
	v_lshl_add_u64 v[0:1], v[0:1], 0, v[26:27]
	v_lshl_or_b32 v3, v4, 8, v26
	v_lshl_add_u64 v[0:1], s[4:5], 0, v[0:1]
	s_mov_b64 s[0:1], 0
	s_mov_b64 s[2:3], 0x3000
	s_movk_i32 s4, 0x17f

	.amdhsa_kernel _Z6pool_kPKfS0_S0_S0_S0_S0_PfS1_
		.amdhsa_group_segment_fixed_size 47872
		.amdhsa_private_segment_fixed_size 0
		.amdhsa_kernarg_size 64
		.amdhsa_user_sgpr_count 2
		.amdhsa_user_sgpr_dispatch_ptr 0
		.amdhsa_user_sgpr_queue_ptr 0
		.amdhsa_user_sgpr_kernarg_segment_ptr 1
		.amdhsa_user_sgpr_dispatch_id 0
		.amdhsa_user_sgpr_kernarg_preload_length 0
		.amdhsa_user_sgpr_kernarg_preload_offset 0
		.amdhsa_user_sgpr_private_segment_size 0
		.amdhsa_uses_dynamic_stack 0
		.amdhsa_enable_private_segment 0
		.amdhsa_system_sgpr_workgroup_id_x 1
		.amdhsa_system_sgpr_workgroup_id_y 1
		.amdhsa_system_sgpr_workgroup_id_z 0
		.amdhsa_system_sgpr_workgroup_info 0
		.amdhsa_system_vgpr_workitem_id 0
		.amdhsa_next_free_vgpr 220
		.amdhsa_next_free_sgpr 96
		.amdhsa_accum_offset 220
		.amdhsa_reserve_vcc 1
		.amdhsa_float_round_mode_32 0
		.amdhsa_float_round_mode_16_64 0
		.amdhsa_float_denorm_mode_32 3
		.amdhsa_float_denorm_mode_16_64 3
		.amdhsa_dx10_clamp 1
		.amdhsa_ieee_mode 1
		.amdhsa_fp16_overflow 0
		.amdhsa_tg_split 0
		.amdhsa_exception_fp_ieee_invalid_op 0
		.amdhsa_exception_fp_denorm_src 0
		.amdhsa_exception_fp_ieee_div_zero 0
		.amdhsa_exception_fp_ieee_overflow 0
		.amdhsa_exception_fp_ieee_underflow 0
		.amdhsa_exception_fp_ieee_inexact 0
		.amdhsa_exception_int_div_zero 0
	.end_amdhsa_kernel

.LBB15_1:
	v_mov_b32_e32 v1, v0
	v_mul_u32_u24_sdwa v4, v1, s1 dst_sel:DWORD dst_unused:UNUSED_PAD src0_sel:WORD_0 src1_sel:DWORD
	v_lshrrev_b32_e32 v8, 23, v4
	v_mul_lo_u16_e32 v4, 0xc0, v8
	v_sub_u16_e32 v4, v1, v4
	v_mad_u64_u32 v[6:7], s[14:15], v8, s10, v[2:3]
	v_lshlrev_b32_e32 v4, 2, v4
	v_lshl_add_u64 v[6:7], v[6:7], 0, v[4:5]
	global_load_dword v100, v[6:7], off
	v_mad_u32_u24 v106, v8, s11, v4
	v_add_u32_e32 v1, 0x100, v0
	v_mul_u32_u24_sdwa v4, v1, s1 dst_sel:DWORD dst_unused:UNUSED_PAD src0_sel:WORD_0 src1_sel:DWORD
	v_lshrrev_b32_e32 v8, 23, v4
	v_mul_lo_u16_e32 v4, 0xc0, v8
	v_sub_u16_e32 v4, v1, v4
	v_mad_u64_u32 v[6:7], s[14:15], v8, s10, v[2:3]
	v_lshlrev_b32_e32 v4, 2, v4
	v_lshl_add_u64 v[6:7], v[6:7], 0, v[4:5]
	global_load_dword v101, v[6:7], off
	v_mad_u32_u24 v107, v8, s11, v4
	v_add_u32_e32 v1, 0x200, v0
	v_mul_u32_u24_sdwa v4, v1, s1 dst_sel:DWORD dst_unused:UNUSED_PAD src0_sel:WORD_0 src1_sel:DWORD
	v_lshrrev_b32_e32 v8, 23, v4
	v_mul_lo_u16_e32 v4, 0xc0, v8
	v_sub_u16_e32 v4, v1, v4
	v_mad_u64_u32 v[6:7], s[14:15], v8, s10, v[2:3]
	v_lshlrev_b32_e32 v4, 2, v4
	v_lshl_add_u64 v[6:7], v[6:7], 0, v[4:5]
	global_load_dword v102, v[6:7], off
	v_mad_u32_u24 v108, v8, s11, v4
	v_add_u32_e32 v1, 0x300, v0
	v_mul_u32_u24_sdwa v4, v1, s1 dst_sel:DWORD dst_unused:UNUSED_PAD src0_sel:WORD_0 src1_sel:DWORD
	v_lshrrev_b32_e32 v8, 23, v4
	v_mul_lo_u16_e32 v4, 0xc0, v8
	v_sub_u16_e32 v4, v1, v4
	v_mad_u64_u32 v[6:7], s[14:15], v8, s10, v[2:3]
	v_lshlrev_b32_e32 v4, 2, v4
	v_lshl_add_u64 v[6:7], v[6:7], 0, v[4:5]
	global_load_dword v103, v[6:7], off
	v_mad_u32_u24 v109, v8, s11, v4
	v_add_u32_e32 v1, 0x400, v0
	v_mul_u32_u24_sdwa v4, v1, s1 dst_sel:DWORD dst_unused:UNUSED_PAD src0_sel:WORD_0 src1_sel:DWORD
	v_lshrrev_b32_e32 v8, 23, v4
	v_mul_lo_u16_e32 v4, 0xc0, v8
	v_sub_u16_e32 v4, v1, v4
	v_mad_u64_u32 v[6:7], s[14:15], v8, s10, v[2:3]
	v_lshlrev_b32_e32 v4, 2, v4
	v_lshl_add_u64 v[6:7], v[6:7], 0, v[4:5]
	global_load_dword v104, v[6:7], off
	v_mad_u32_u24 v110, v8, s11, v4
	v_add_u32_e32 v1, 0x500, v0
	v_mul_u32_u24_sdwa v4, v1, s1 dst_sel:DWORD dst_unused:UNUSED_PAD src0_sel:WORD_0 src1_sel:DWORD
	v_lshrrev_b32_e32 v8, 23, v4
	v_mul_lo_u16_e32 v4, 0xc0, v8
	v_sub_u16_e32 v4, v1, v4
	v_mad_u64_u32 v[6:7], s[14:15], v8, s10, v[2:3]
	v_lshlrev_b32_e32 v4, 2, v4
	v_lshl_add_u64 v[6:7], v[6:7], 0, v[4:5]
	global_load_dword v105, v[6:7], off
	v_mad_u32_u24 v111, v8, s11, v4
	s_or_b64 exec, exec, s[4:5]
	s_lshl_b32 s4, s2, 6
	s_mul_hi_i32 s1, s0, 0xc00
	s_mulk_i32 s0, 0xc00
	s_ashr_i32 s5, s4, 31
	s_add_u32 s2, s6, s0
	s_addc_u32 s6, s7, s1
	s_lshl_b64 s[0:1], s[4:5], 2
	s_add_u32 s4, s2, s0
	v_lshlrev_b32_e32 v2, 4, v0
	v_lshrrev_b32_e32 v1, 4, v0
	s_addc_u32 s5, s6, s1
	v_and_b32_e32 v50, 0xf0, v2
	v_mov_b32_e32 v51, 0
	v_lshl_add_u64 v[42:43], s[4:5], 0, v[50:51]
	v_mul_u32_u24_e32 v30, 0xc00, v1
	v_mov_b32_e32 v31, v51
	v_lshl_add_u64 v[10:11], v[42:43], 0, v[30:31]
	s_mov_b32 s4, 0xc000
	v_add_co_u32_e32 v12, vcc, s4, v10
	s_mov_b32 s5, 0x18000
	s_nop 0
	v_addc_co_u32_e32 v13, vcc, 0, v11, vcc
	v_add_co_u32_e32 v16, vcc, s5, v10
	global_load_dwordx4 v[46:49], v[10:11], off
	s_mov_b32 s6, 0x24000
	v_addc_co_u32_e32 v17, vcc, 0, v11, vcc
	s_movk_i32 s2, 0xc00
	v_mov_b32_e32 v2, 0x3c000
	v_mov_b32_e32 v3, 0x48000
	v_mov_b32_e32 v4, 0x54000
	v_mov_b32_e32 v5, 0x6c000
	v_add_co_u32_e32 v10, vcc, s6, v10
	v_mad_u32_u24 v18, v1, s2, v2
	v_mad_u32_u24 v22, v1, s2, v3
	v_mad_u32_u24 v26, v1, s2, v4
	v_mad_u32_u24 v34, v1, s2, v5
	global_load_dwordx4 v[2:5], v[12:13], off
	global_load_dwordx4 v[6:9], v[16:17], off
	v_addc_co_u32_e32 v11, vcc, 0, v11, vcc
	global_load_dwordx4 v[10:13], v[10:11], off
	v_mov_b32_e32 v15, v51
	v_or_b32_e32 v14, 0x30000, v30
	v_mov_b32_e32 v19, v51
	v_lshl_add_u64 v[14:15], v[42:43], 0, v[14:15]
	v_mov_b32_e32 v23, v51
	global_load_dwordx4 v[14:17], v[14:15], off
	v_lshl_add_u64 v[18:19], v[42:43], 0, v[18:19]
	v_mov_b32_e32 v24, 0x78000
	v_mov_b32_e32 v27, v51
	global_load_dwordx4 v[18:21], v[18:19], off
	v_lshl_add_u64 v[22:23], v[42:43], 0, v[22:23]
	v_mad_u32_u24 v36, v1, s2, v24
	global_load_dwordx4 v[22:25], v[22:23], off
	v_lshl_add_u64 v[26:27], v[42:43], 0, v[26:27]
	global_load_dwordx4 v[26:29], v[26:27], off
	v_or_b32_e32 v30, 0x60000, v30
	v_mov_b32_e32 v35, v51
	v_lshl_add_u64 v[30:31], v[42:43], 0, v[30:31]
	v_mov_b32_e32 v54, 0x84000
	v_mov_b32_e32 v37, v51
	global_load_dwordx4 v[30:33], v[30:31], off
	v_lshl_add_u64 v[44:45], v[42:43], 0, v[34:35]
	v_lshl_add_u64 v[52:53], v[42:43], 0, v[36:37]
	global_load_dwordx4 v[34:37], v[44:45], off
	global_load_dwordx4 v[38:41], v[52:53], off
	v_mad_u32_u24 v44, v1, s2, v54
	v_mov_b32_e32 v45, v51
	v_lshl_add_u64 v[42:43], v[42:43], 0, v[44:45]
	global_load_dwordx4 v[42:45], v[42:43], off
	s_waitcnt vmcnt(12)
	ds_write_b32 v106, v100 offset:32768
	ds_write_b32 v107, v101 offset:32768
	ds_write_b32 v108, v102 offset:32768
	ds_write_b32 v109, v103 offset:32768
	ds_write_b32 v110, v104 offset:32768
	ds_write_b32 v111, v105 offset:32768
	s_waitcnt lgkmcnt(0)
	s_barrier
	v_lshlrev_b32_e32 v54, 2, v1
	v_add_u32_e32 v99, 0x8000, v54
	v_add_u32_e32 v125, 0x9000, v54
	ds_read2_b32 v[52:53], v99 offset1:16
	ds_read2_b32 v[80:81], v125 offset0:128 offset1:144
	v_add_u32_e32 v101, 0x8400, v54
	v_add_u32_e32 v103, 0x8800, v54
	v_add_u32_e32 v124, 0x8c00, v54
	v_add_u32_e32 v126, 0x9400, v54
	ds_read2_b32 v[58:59], v99 offset0:192 offset1:208
	ds_read2_b32 v[60:61], v101 offset0:128 offset1:144
	ds_read2_b32 v[68:69], v103 offset0:64 offset1:80
	ds_read2_b32 v[70:71], v124 offset1:16
	ds_read2_b32 v[78:79], v124 offset0:192 offset1:208
	ds_read2_b32 v[82:83], v126 offset0:64 offset1:80
	s_waitcnt lgkmcnt(4)
	v_mov_b32_e32 v100, v61
	v_lshl_or_b32 v1, v1, 11, v50
	v_mov_b32_e32 v98, v59
	s_waitcnt lgkmcnt(3)
	v_mov_b32_e32 v102, v69
	s_movk_i32 s4, 0x200
	v_cmp_gt_u32_e32 vcc, s4, v0
	s_waitcnt vmcnt(11)
	v_pk_fma_f32 v[64:65], v[46:47], v[52:53], 0 op_sel_hi:[1,0,0]
	v_pk_fma_f32 v[74:75], v[48:49], v[52:53], 0 op_sel_hi:[1,0,0]
	v_pk_fma_f32 v[62:63], v[46:47], v[80:81], 0 op_sel_hi:[1,0,0]
	v_pk_fma_f32 v[56:57], v[48:49], v[80:81], 0 op_sel_hi:[1,0,0]
	v_mov_b32_e32 v80, v53
	v_pk_fma_f32 v[84:85], v[46:47], v[58:59], 0 op_sel_hi:[1,0,0]
	v_pk_fma_f32 v[86:87], v[48:49], v[58:59], 0 op_sel_hi:[1,0,0]
	v_pk_fma_f32 v[88:89], v[46:47], v[60:61], 0 op_sel_hi:[1,0,0]
	v_pk_fma_f32 v[90:91], v[48:49], v[60:61], 0 op_sel_hi:[1,0,0]
	v_pk_fma_f32 v[92:93], v[46:47], v[68:69], 0 op_sel_hi:[1,0,0]
	v_pk_fma_f32 v[94:95], v[48:49], v[68:69], 0 op_sel_hi:[1,0,0]
	s_waitcnt lgkmcnt(2)
	v_pk_fma_f32 v[96:97], v[46:47], v[70:71], 0 op_sel_hi:[1,0,0]
	v_pk_fma_f32 v[76:77], v[48:49], v[70:71], 0 op_sel_hi:[1,0,0]
	s_waitcnt lgkmcnt(1)
	v_pk_fma_f32 v[72:73], v[46:47], v[78:79], 0 op_sel_hi:[1,0,0]
	s_waitcnt vmcnt(10)
	v_pk_fma_f32 v[64:65], v[2:3], v[80:81], v[64:65] op_sel_hi:[1,0,1]
	v_pk_fma_f32 v[74:75], v[4:5], v[80:81], v[74:75] op_sel_hi:[1,0,1]
	v_pk_fma_f32 v[66:67], v[48:49], v[78:79], 0 op_sel_hi:[1,0,0]
	s_waitcnt lgkmcnt(0)
	v_pk_fma_f32 v[54:55], v[46:47], v[82:83], 0 op_sel_hi:[1,0,0]
	v_pk_fma_f32 v[46:47], v[48:49], v[82:83], 0 op_sel_hi:[1,0,0]
	v_mov_b32_e32 v78, v71
	v_mov_b32_e32 v48, v83
	ds_read2_b32 v[82:83], v99 offset0:32 offset1:48
	ds_read2_b32 v[104:105], v99 offset0:224 offset1:240
	ds_read2_b32 v[106:107], v101 offset0:160 offset1:176
	ds_read2_b32 v[108:109], v103 offset0:96 offset1:112
	ds_read2_b32 v[110:111], v124 offset0:32 offset1:48
	ds_read2_b32 v[70:71], v124 offset0:224 offset1:240
	ds_read2_b32 v[60:61], v125 offset0:160 offset1:176
	ds_read2_b32 v[52:53], v126 offset0:96 offset1:112
	ds_read2_b32 v[112:113], v99 offset0:64 offset1:80
	ds_read2_b32 v[114:115], v101 offset1:16
	ds_read2_b32 v[116:117], v101 offset0:192 offset1:208
	s_waitcnt vmcnt(9) lgkmcnt(10)
	v_pk_fma_f32 v[64:65], v[6:7], v[82:83], v[64:65] op_sel_hi:[1,0,1]
	v_pk_fma_f32 v[74:75], v[8:9], v[82:83], v[74:75] op_sel_hi:[1,0,1]
	v_mov_b32_e32 v80, v83
	v_mov_b32_e32 v58, v81
	s_waitcnt vmcnt(8)
	v_pk_fma_f32 v[64:65], v[10:11], v[80:81], v[64:65] op_sel_hi:[1,0,1]
	v_pk_fma_f32 v[74:75], v[12:13], v[80:81], v[74:75] op_sel_hi:[1,0,1]
	ds_read2_b32 v[80:81], v99 offset0:96 offset1:112
	s_waitcnt vmcnt(7) lgkmcnt(3)
	v_pk_fma_f32 v[64:65], v[14:15], v[112:113], v[64:65] op_sel_hi:[1,0,1]
	v_pk_fma_f32 v[74:75], v[16:17], v[112:113], v[74:75] op_sel_hi:[1,0,1]
	v_mov_b32_e32 v82, v113
	s_waitcnt vmcnt(6)
	v_pk_fma_f32 v[64:65], v[18:19], v[82:83], v[64:65] op_sel_hi:[1,0,1]
	v_pk_fma_f32 v[74:75], v[20:21], v[82:83], v[74:75] op_sel_hi:[1,0,1]
	ds_read2_b32 v[82:83], v99 offset0:128 offset1:144
	s_waitcnt vmcnt(5) lgkmcnt(1)
	v_pk_fma_f32 v[64:65], v[22:23], v[80:81], v[64:65] op_sel_hi:[1,0,1]
	v_pk_fma_f32 v[74:75], v[24:25], v[80:81], v[74:75] op_sel_hi:[1,0,1]
	v_mov_b32_e32 v80, v81
	s_waitcnt vmcnt(4)
	v_pk_fma_f32 v[64:65], v[26:27], v[80:81], v[64:65] op_sel_hi:[1,0,1]
	v_pk_fma_f32 v[74:75], v[28:29], v[80:81], v[74:75] op_sel_hi:[1,0,1]
	ds_read2_b32 v[80:81], v99 offset0:160 offset1:176
	s_waitcnt vmcnt(3) lgkmcnt(1)
	v_pk_fma_f32 v[64:65], v[30:31], v[82:83], v[64:65] op_sel_hi:[1,0,1]
	v_pk_fma_f32 v[74:75], v[32:33], v[82:83], v[74:75] op_sel_hi:[1,0,1]
	v_mov_b32_e32 v82, v83
	s_waitcnt vmcnt(2)
	v_pk_fma_f32 v[64:65], v[34:35], v[82:83], v[64:65] op_sel_hi:[1,0,1]
	v_pk_fma_f32 v[74:75], v[36:37], v[82:83], v[74:75] op_sel_hi:[1,0,1]
	s_waitcnt vmcnt(1) lgkmcnt(0)
	v_pk_fma_f32 v[64:65], v[38:39], v[80:81], v[64:65] op_sel_hi:[1,0,1]
	v_mov_b32_e32 v82, v81
	v_pk_fma_f32 v[74:75], v[40:41], v[80:81], v[74:75] op_sel_hi:[1,0,1]
	s_waitcnt vmcnt(0)
	v_pk_fma_f32 v[80:81], v[42:43], v[82:83], v[64:65] op_sel_hi:[1,0,1]
	v_pk_fma_f32 v[82:83], v[44:45], v[82:83], v[74:75] op_sel_hi:[1,0,1]
	ds_read2_b32 v[118:119], v103 offset0:128 offset1:144
	ds_read2_b32 v[112:113], v124 offset0:64 offset1:80
	ds_read2_b32 v[120:121], v125 offset1:16
	ds_write_b128 v1, v[80:83]
	ds_read2_b32 v[74:75], v125 offset0:192 offset1:208
	ds_read2_b32 v[64:65], v126 offset0:128 offset1:144
	v_pk_fma_f32 v[80:81], v[2:3], v[98:99], v[84:85] op_sel_hi:[1,0,1]
	v_pk_fma_f32 v[82:83], v[4:5], v[98:99], v[86:87] op_sel_hi:[1,0,1]
	ds_read2_b32 v[84:85], v101 offset0:32 offset1:48
	v_pk_fma_f32 v[80:81], v[6:7], v[104:105], v[80:81] op_sel_hi:[1,0,1]
	v_pk_fma_f32 v[82:83], v[8:9], v[104:105], v[82:83] op_sel_hi:[1,0,1]
	v_mov_b32_e32 v50, v105
	v_pk_fma_f32 v[80:81], v[10:11], v[50:51], v[80:81] op_sel_hi:[1,0,1]
	v_pk_fma_f32 v[82:83], v[12:13], v[50:51], v[82:83] op_sel_hi:[1,0,1]
	v_pk_fma_f32 v[80:81], v[14:15], v[114:115], v[80:81] op_sel_hi:[1,0,1]
	v_pk_fma_f32 v[82:83], v[16:17], v[114:115], v[82:83] op_sel_hi:[1,0,1]
	v_mov_b32_e32 v50, v115
	ds_read2_b32 v[98:99], v101 offset0:64 offset1:80
	v_pk_fma_f32 v[80:81], v[18:19], v[50:51], v[80:81] op_sel_hi:[1,0,1]
	v_pk_fma_f32 v[82:83], v[20:21], v[50:51], v[82:83] op_sel_hi:[1,0,1]
	ds_read2_b32 v[86:87], v101 offset0:224 offset1:240
	s_waitcnt lgkmcnt(2)
	v_pk_fma_f32 v[80:81], v[22:23], v[84:85], v[80:81] op_sel_hi:[1,0,1]
	v_pk_fma_f32 v[82:83], v[24:25], v[84:85], v[82:83] op_sel_hi:[1,0,1]
	v_mov_b32_e32 v50, v85
	ds_read2_b32 v[84:85], v103 offset0:160 offset1:176
	ds_read2_b32 v[104:105], v101 offset0:96 offset1:112
	v_pk_fma_f32 v[80:81], v[26:27], v[50:51], v[80:81] op_sel_hi:[1,0,1]
	v_pk_fma_f32 v[82:83], v[28:29], v[50:51], v[82:83] op_sel_hi:[1,0,1]
	s_waitcnt lgkmcnt(3)
	v_pk_fma_f32 v[80:81], v[30:31], v[98:99], v[80:81] op_sel_hi:[1,0,1]
	v_pk_fma_f32 v[82:83], v[32:33], v[98:99], v[82:83] op_sel_hi:[1,0,1]
	v_mov_b32_e32 v50, v99
	v_pk_fma_f32 v[80:81], v[34:35], v[50:51], v[80:81] op_sel_hi:[1,0,1]
	v_pk_fma_f32 v[82:83], v[36:37], v[50:51], v[82:83] op_sel_hi:[1,0,1]
	s_waitcnt lgkmcnt(0)
	v_pk_fma_f32 v[80:81], v[38:39], v[104:105], v[80:81] op_sel_hi:[1,0,1]
	v_mov_b32_e32 v50, v105
	v_pk_fma_f32 v[82:83], v[40:41], v[104:105], v[82:83] op_sel_hi:[1,0,1]
	v_pk_fma_f32 v[80:81], v[42:43], v[50:51], v[80:81] op_sel_hi:[1,0,1]
	v_pk_fma_f32 v[82:83], v[44:45], v[50:51], v[82:83] op_sel_hi:[1,0,1]
	ds_read2_b32 v[98:99], v124 offset0:96 offset1:112
	ds_read2_b32 v[104:105], v125 offset0:32 offset1:48
	ds_write_b128 v1, v[80:83] offset:256
	v_pk_fma_f32 v[80:81], v[2:3], v[100:101], v[88:89] op_sel_hi:[1,0,1]
	v_pk_fma_f32 v[82:83], v[4:5], v[100:101], v[90:91] op_sel_hi:[1,0,1]
	v_pk_fma_f32 v[80:81], v[6:7], v[106:107], v[80:81] op_sel_hi:[1,0,1]
	v_pk_fma_f32 v[82:83], v[8:9], v[106:107], v[82:83] op_sel_hi:[1,0,1]
	v_mov_b32_e32 v50, v107
	v_pk_fma_f32 v[80:81], v[10:11], v[50:51], v[80:81] op_sel_hi:[1,0,1]
	v_pk_fma_f32 v[82:83], v[12:13], v[50:51], v[82:83] op_sel_hi:[1,0,1]
	ds_read2_b32 v[114:115], v125 offset0:224 offset1:240
	ds_read2_b32 v[122:123], v126 offset0:160 offset1:176
	ds_read2_b32 v[88:89], v103 offset1:16
	v_pk_fma_f32 v[80:81], v[14:15], v[116:117], v[80:81] op_sel_hi:[1,0,1]
	v_pk_fma_f32 v[82:83], v[16:17], v[116:117], v[82:83] op_sel_hi:[1,0,1]
	v_mov_b32_e32 v50, v117
	v_pk_fma_f32 v[80:81], v[18:19], v[50:51], v[80:81] op_sel_hi:[1,0,1]
	v_pk_fma_f32 v[82:83], v[20:21], v[50:51], v[82:83] op_sel_hi:[1,0,1]
	v_pk_fma_f32 v[80:81], v[22:23], v[86:87], v[80:81] op_sel_hi:[1,0,1]
	v_pk_fma_f32 v[82:83], v[24:25], v[86:87], v[82:83] op_sel_hi:[1,0,1]
	v_mov_b32_e32 v50, v87
	ds_read2_b32 v[86:87], v103 offset0:32 offset1:48
	v_pk_fma_f32 v[80:81], v[26:27], v[50:51], v[80:81] op_sel_hi:[1,0,1]
	v_pk_fma_f32 v[82:83], v[28:29], v[50:51], v[82:83] op_sel_hi:[1,0,1]
	s_waitcnt lgkmcnt(1)
	v_pk_fma_f32 v[80:81], v[30:31], v[88:89], v[80:81] op_sel_hi:[1,0,1]
	v_pk_fma_f32 v[82:83], v[32:33], v[88:89], v[82:83] op_sel_hi:[1,0,1]
	v_mov_b32_e32 v50, v89
	v_pk_fma_f32 v[80:81], v[34:35], v[50:51], v[80:81] op_sel_hi:[1,0,1]
	v_pk_fma_f32 v[82:83], v[36:37], v[50:51], v[82:83] op_sel_hi:[1,0,1]
	s_waitcnt lgkmcnt(0)
	v_pk_fma_f32 v[80:81], v[38:39], v[86:87], v[80:81] op_sel_hi:[1,0,1]
	v_mov_b32_e32 v50, v87
	v_pk_fma_f32 v[82:83], v[40:41], v[86:87], v[82:83] op_sel_hi:[1,0,1]
	v_pk_fma_f32 v[80:81], v[42:43], v[50:51], v[80:81] op_sel_hi:[1,0,1]
	v_pk_fma_f32 v[82:83], v[44:45], v[50:51], v[82:83] op_sel_hi:[1,0,1]
	ds_read2_b32 v[90:91], v103 offset0:192 offset1:208
	ds_read2_b32 v[100:101], v124 offset0:128 offset1:144
	ds_read2_b32 v[86:87], v125 offset0:64 offset1:80
	ds_read2_b32 v[88:89], v126 offset1:16
	ds_write_b128 v1, v[80:83] offset:512
	v_pk_fma_f32 v[80:81], v[2:3], v[102:103], v[92:93] op_sel_hi:[1,0,1]
	v_pk_fma_f32 v[92:93], v[4:5], v[102:103], v[94:95] op_sel_hi:[1,0,1]
	v_pk_fma_f32 v[80:81], v[6:7], v[108:109], v[80:81] op_sel_hi:[1,0,1]
	v_pk_fma_f32 v[92:93], v[8:9], v[108:109], v[92:93] op_sel_hi:[1,0,1]
	v_mov_b32_e32 v50, v109
	v_pk_fma_f32 v[80:81], v[10:11], v[50:51], v[80:81] op_sel_hi:[1,0,1]
	v_pk_fma_f32 v[92:93], v[12:13], v[50:51], v[92:93] op_sel_hi:[1,0,1]
	v_pk_fma_f32 v[80:81], v[14:15], v[118:119], v[80:81] op_sel_hi:[1,0,1]
	v_pk_fma_f32 v[92:93], v[16:17], v[118:119], v[92:93] op_sel_hi:[1,0,1]
	v_mov_b32_e32 v50, v119
	v_pk_fma_f32 v[80:81], v[18:19], v[50:51], v[80:81] op_sel_hi:[1,0,1]
	v_pk_fma_f32 v[92:93], v[20:21], v[50:51], v[92:93] op_sel_hi:[1,0,1]
	ds_read2_b32 v[106:107], v126 offset0:192 offset1:208
	ds_read2_b32 v[82:83], v103 offset0:224 offset1:240
	ds_read2_b32 v[116:117], v124 offset0:160 offset1:176
	v_pk_fma_f32 v[80:81], v[22:23], v[84:85], v[80:81] op_sel_hi:[1,0,1]
	v_mov_b32_e32 v50, v85
	v_pk_fma_f32 v[84:85], v[24:25], v[84:85], v[92:93] op_sel_hi:[1,0,1]
	v_pk_fma_f32 v[80:81], v[26:27], v[50:51], v[80:81] op_sel_hi:[1,0,1]
	v_pk_fma_f32 v[84:85], v[28:29], v[50:51], v[84:85] op_sel_hi:[1,0,1]
	s_waitcnt lgkmcnt(7)
	v_pk_fma_f32 v[80:81], v[30:31], v[90:91], v[80:81] op_sel_hi:[1,0,1]
	v_mov_b32_e32 v92, v91
	v_pk_fma_f32 v[84:85], v[32:33], v[90:91], v[84:85] op_sel_hi:[1,0,1]
	v_pk_fma_f32 v[80:81], v[34:35], v[92:93], v[80:81] op_sel_hi:[1,0,1]
	v_pk_fma_f32 v[84:85], v[36:37], v[92:93], v[84:85] op_sel_hi:[1,0,1]
	s_waitcnt lgkmcnt(1)
	v_pk_fma_f32 v[80:81], v[38:39], v[82:83], v[80:81] op_sel_hi:[1,0,1]
	v_mov_b32_e32 v50, v83
	v_pk_fma_f32 v[82:83], v[40:41], v[82:83], v[84:85] op_sel_hi:[1,0,1]
	v_pk_fma_f32 v[80:81], v[42:43], v[50:51], v[80:81] op_sel_hi:[1,0,1]
	v_pk_fma_f32 v[82:83], v[44:45], v[50:51], v[82:83] op_sel_hi:[1,0,1]
	ds_read2_b32 v[94:95], v125 offset0:96 offset1:112
	ds_read2_b32 v[102:103], v126 offset0:32 offset1:48
	ds_read2_b32 v[108:109], v126 offset0:224 offset1:240
	ds_write_b128 v1, v[80:83] offset:768
	v_pk_fma_f32 v[80:81], v[2:3], v[78:79], v[96:97] op_sel_hi:[1,0,1]
	v_pk_fma_f32 v[76:77], v[4:5], v[78:79], v[76:77] op_sel_hi:[1,0,1]
	v_pk_fma_f32 v[80:81], v[6:7], v[110:111], v[80:81] op_sel_hi:[1,0,1]
	v_mov_b32_e32 v50, v111
	v_pk_fma_f32 v[76:77], v[8:9], v[110:111], v[76:77] op_sel_hi:[1,0,1]
	v_pk_fma_f32 v[80:81], v[10:11], v[50:51], v[80:81] op_sel_hi:[1,0,1]
	v_pk_fma_f32 v[76:77], v[12:13], v[50:51], v[76:77] op_sel_hi:[1,0,1]
	v_pk_fma_f32 v[80:81], v[14:15], v[112:113], v[80:81] op_sel_hi:[1,0,1]
	v_mov_b32_e32 v82, v113
	v_pk_fma_f32 v[76:77], v[16:17], v[112:113], v[76:77] op_sel_hi:[1,0,1]
	v_pk_fma_f32 v[80:81], v[18:19], v[82:83], v[80:81] op_sel_hi:[1,0,1]
	v_pk_fma_f32 v[76:77], v[20:21], v[82:83], v[76:77] op_sel_hi:[1,0,1]
	v_mov_b32_e32 v68, v79
	v_pk_fma_f32 v[80:81], v[22:23], v[98:99], v[80:81] op_sel_hi:[1,0,1]
	v_mov_b32_e32 v84, v99
	v_pk_fma_f32 v[76:77], v[24:25], v[98:99], v[76:77] op_sel_hi:[1,0,1]
	v_pk_fma_f32 v[80:81], v[26:27], v[84:85], v[80:81] op_sel_hi:[1,0,1]
	v_pk_fma_f32 v[76:77], v[28:29], v[84:85], v[76:77] op_sel_hi:[1,0,1]
	v_pk_fma_f32 v[72:73], v[2:3], v[68:69], v[72:73] op_sel_hi:[1,0,1]
	v_pk_fma_f32 v[80:81], v[30:31], v[100:101], v[80:81] op_sel_hi:[1,0,1]
	v_mov_b32_e32 v90, v101
	v_pk_fma_f32 v[76:77], v[32:33], v[100:101], v[76:77] op_sel_hi:[1,0,1]
	v_pk_fma_f32 v[72:73], v[6:7], v[70:71], v[72:73] op_sel_hi:[1,0,1]
	v_mov_b32_e32 v50, v71
	v_pk_fma_f32 v[66:67], v[4:5], v[68:69], v[66:67] op_sel_hi:[1,0,1]
	v_pk_fma_f32 v[80:81], v[34:35], v[90:91], v[80:81] op_sel_hi:[1,0,1]
	v_pk_fma_f32 v[76:77], v[36:37], v[90:91], v[76:77] op_sel_hi:[1,0,1]
	v_pk_fma_f32 v[72:73], v[10:11], v[50:51], v[72:73] op_sel_hi:[1,0,1]
	v_pk_fma_f32 v[66:67], v[8:9], v[70:71], v[66:67] op_sel_hi:[1,0,1]
	s_waitcnt lgkmcnt(4)
	v_pk_fma_f32 v[80:81], v[38:39], v[116:117], v[80:81] op_sel_hi:[1,0,1]
	v_mov_b32_e32 v92, v117
	v_pk_fma_f32 v[76:77], v[40:41], v[116:117], v[76:77] op_sel_hi:[1,0,1]
	v_pk_fma_f32 v[72:73], v[14:15], v[120:121], v[72:73] op_sel_hi:[1,0,1]
	v_mov_b32_e32 v78, v121
	v_pk_fma_f32 v[66:67], v[12:13], v[50:51], v[66:67] op_sel_hi:[1,0,1]
	v_pk_fma_f32 v[62:63], v[2:3], v[58:59], v[62:63] op_sel_hi:[1,0,1]
	v_pk_fma_f32 v[56:57], v[4:5], v[58:59], v[56:57] op_sel_hi:[1,0,1]
	v_pk_fma_f32 v[2:3], v[2:3], v[48:49], v[54:55] op_sel_hi:[1,0,1]
	v_pk_fma_f32 v[4:5], v[4:5], v[48:49], v[46:47] op_sel_hi:[1,0,1]
	v_pk_fma_f32 v[80:81], v[42:43], v[92:93], v[80:81] op_sel_hi:[1,0,1]
	v_pk_fma_f32 v[82:83], v[44:45], v[92:93], v[76:77] op_sel_hi:[1,0,1]
	v_pk_fma_f32 v[72:73], v[18:19], v[78:79], v[72:73] op_sel_hi:[1,0,1]
	v_pk_fma_f32 v[66:67], v[16:17], v[120:121], v[66:67] op_sel_hi:[1,0,1]
	v_pk_fma_f32 v[62:63], v[6:7], v[60:61], v[62:63] op_sel_hi:[1,0,1]
	v_mov_b32_e32 v50, v61
	v_pk_fma_f32 v[56:57], v[8:9], v[60:61], v[56:57] op_sel_hi:[1,0,1]
	v_pk_fma_f32 v[2:3], v[6:7], v[52:53], v[2:3] op_sel_hi:[1,0,1]
	v_mov_b32_e32 v6, v53
	v_pk_fma_f32 v[4:5], v[8:9], v[52:53], v[4:5] op_sel_hi:[1,0,1]
	ds_write_b128 v1, v[80:83] offset:1024
	v_pk_fma_f32 v[72:73], v[22:23], v[104:105], v[72:73] op_sel_hi:[1,0,1]
	v_mov_b32_e32 v80, v105
	v_pk_fma_f32 v[66:67], v[20:21], v[78:79], v[66:67] op_sel_hi:[1,0,1]
	v_pk_fma_f32 v[62:63], v[10:11], v[50:51], v[62:63] op_sel_hi:[1,0,1]
	v_pk_fma_f32 v[56:57], v[12:13], v[50:51], v[56:57] op_sel_hi:[1,0,1]
	v_pk_fma_f32 v[2:3], v[10:11], v[6:7], v[2:3] op_sel_hi:[1,0,1]
	v_pk_fma_f32 v[4:5], v[12:13], v[6:7], v[4:5] op_sel_hi:[1,0,1]
	v_pk_fma_f32 v[72:73], v[26:27], v[80:81], v[72:73] op_sel_hi:[1,0,1]
	v_pk_fma_f32 v[66:67], v[24:25], v[104:105], v[66:67] op_sel_hi:[1,0,1]
	v_pk_fma_f32 v[62:63], v[14:15], v[74:75], v[62:63] op_sel_hi:[1,0,1]
	v_mov_b32_e32 v68, v75
	v_pk_fma_f32 v[56:57], v[16:17], v[74:75], v[56:57] op_sel_hi:[1,0,1]
	v_pk_fma_f32 v[2:3], v[14:15], v[64:65], v[2:3] op_sel_hi:[1,0,1]
	v_mov_b32_e32 v10, v65
	v_pk_fma_f32 v[4:5], v[16:17], v[64:65], v[4:5] op_sel_hi:[1,0,1]
	v_pk_fma_f32 v[72:73], v[30:31], v[86:87], v[72:73] op_sel_hi:[1,0,1]
	v_mov_b32_e32 v82, v87
	v_pk_fma_f32 v[66:67], v[28:29], v[80:81], v[66:67] op_sel_hi:[1,0,1]
	v_pk_fma_f32 v[62:63], v[18:19], v[68:69], v[62:63] op_sel_hi:[1,0,1]
	v_pk_fma_f32 v[56:57], v[20:21], v[68:69], v[56:57] op_sel_hi:[1,0,1]
	v_pk_fma_f32 v[2:3], v[18:19], v[10:11], v[2:3] op_sel_hi:[1,0,1]
	v_pk_fma_f32 v[4:5], v[20:21], v[10:11], v[4:5] op_sel_hi:[1,0,1]
	v_pk_fma_f32 v[72:73], v[34:35], v[82:83], v[72:73] op_sel_hi:[1,0,1]
	v_pk_fma_f32 v[66:67], v[32:33], v[86:87], v[66:67] op_sel_hi:[1,0,1]
	v_pk_fma_f32 v[62:63], v[22:23], v[114:115], v[62:63] op_sel_hi:[1,0,1]
	v_mov_b32_e32 v70, v115
	v_pk_fma_f32 v[56:57], v[24:25], v[114:115], v[56:57] op_sel_hi:[1,0,1]
	v_pk_fma_f32 v[2:3], v[22:23], v[122:123], v[2:3] op_sel_hi:[1,0,1]
	v_mov_b32_e32 v14, v123
	v_pk_fma_f32 v[4:5], v[24:25], v[122:123], v[4:5] op_sel_hi:[1,0,1]
	s_waitcnt lgkmcnt(4)
	v_pk_fma_f32 v[72:73], v[38:39], v[94:95], v[72:73] op_sel_hi:[1,0,1]
	v_mov_b32_e32 v84, v95
	v_pk_fma_f32 v[66:67], v[36:37], v[82:83], v[66:67] op_sel_hi:[1,0,1]
	v_pk_fma_f32 v[62:63], v[26:27], v[70:71], v[62:63] op_sel_hi:[1,0,1]
	v_pk_fma_f32 v[56:57], v[28:29], v[70:71], v[56:57] op_sel_hi:[1,0,1]
	v_pk_fma_f32 v[2:3], v[26:27], v[14:15], v[2:3] op_sel_hi:[1,0,1]
	v_pk_fma_f32 v[4:5], v[28:29], v[14:15], v[4:5] op_sel_hi:[1,0,1]
	v_pk_fma_f32 v[76:77], v[42:43], v[84:85], v[72:73] op_sel_hi:[1,0,1]
	v_pk_fma_f32 v[66:67], v[40:41], v[94:95], v[66:67] op_sel_hi:[1,0,1]
	v_pk_fma_f32 v[62:63], v[30:31], v[88:89], v[62:63] op_sel_hi:[1,0,1]
	v_mov_b32_e32 v72, v89
	v_pk_fma_f32 v[56:57], v[32:33], v[88:89], v[56:57] op_sel_hi:[1,0,1]
	v_pk_fma_f32 v[2:3], v[30:31], v[106:107], v[2:3] op_sel_hi:[1,0,1]
	v_mov_b32_e32 v18, v107
	v_pk_fma_f32 v[4:5], v[32:33], v[106:107], v[4:5] op_sel_hi:[1,0,1]
	v_pk_fma_f32 v[78:79], v[44:45], v[84:85], v[66:67] op_sel_hi:[1,0,1]
	v_pk_fma_f32 v[62:63], v[34:35], v[72:73], v[62:63] op_sel_hi:[1,0,1]
	v_pk_fma_f32 v[56:57], v[36:37], v[72:73], v[56:57] op_sel_hi:[1,0,1]
	v_pk_fma_f32 v[2:3], v[34:35], v[18:19], v[2:3] op_sel_hi:[1,0,1]
	v_pk_fma_f32 v[4:5], v[36:37], v[18:19], v[4:5] op_sel_hi:[1,0,1]
	ds_write_b128 v1, v[76:79] offset:1280
	s_waitcnt lgkmcnt(4)
	v_pk_fma_f32 v[62:63], v[38:39], v[102:103], v[62:63] op_sel_hi:[1,0,1]
	v_mov_b32_e32 v76, v103
	v_pk_fma_f32 v[56:57], v[40:41], v[102:103], v[56:57] op_sel_hi:[1,0,1]
	s_waitcnt lgkmcnt(3)
	v_pk_fma_f32 v[2:3], v[38:39], v[108:109], v[2:3] op_sel_hi:[1,0,1]
	v_mov_b32_e32 v22, v109
	v_pk_fma_f32 v[4:5], v[40:41], v[108:109], v[4:5] op_sel_hi:[1,0,1]
	v_pk_fma_f32 v[66:67], v[42:43], v[76:77], v[62:63] op_sel_hi:[1,0,1]
	v_pk_fma_f32 v[68:69], v[44:45], v[76:77], v[56:57] op_sel_hi:[1,0,1]
	v_pk_fma_f32 v[2:3], v[42:43], v[22:23], v[2:3] op_sel_hi:[1,0,1]
	v_pk_fma_f32 v[4:5], v[44:45], v[22:23], v[4:5] op_sel_hi:[1,0,1]
	ds_write_b128 v1, v[66:69] offset:1536
	ds_write_b128 v1, v[2:5] offset:1792
	s_waitcnt lgkmcnt(0)
	s_barrier
	s_and_saveexec_b64 s[4:5], vcc
	s_cbranch_execz .LBB15_5
	s_mul_hi_i32 s4, s3, 0x6000
	s_mulk_i32 s3, 0x6000
	s_add_u32 s0, s0, s3
	v_and_b32_e32 v1, 63, v0
	s_addc_u32 s1, s1, s4
	v_or_b32_e32 v2, 0xffffff00, v0
	v_lshrrev_b32_e32 v4, 6, v0
	v_lshlrev_b32_e32 v50, 2, v1
	v_mov_b64_e32 v[0:1], s[0:1]
	v_mad_u64_u32 v[0:1], s[0:1], v4, s2, v[0:1]
	v_lshl_add_u64 v[0:1], v[0:1], 0, v[50:51]
	v_lshl_or_b32 v3, v4, 8, v50
	v_lshl_add_u64 v[0:1], s[8:9], 0, v[0:1]
	s_mov_b64 s[0:1], 0
	s_mov_b64 s[2:3], 0x3000

amdhsa.kernels:
  - .agpr_count:     0
    .args:
      - .address_space:  global
        .offset:         0
        .size:           8
        .value_kind:     global_buffer
    .group_segment_fixed_size: 0
    .kernarg_segment_align: 8
    .kernarg_segment_size: 8
    .language:       OpenCL C
    .language_version:
      - 2
      - 0
    .max_flat_workgroup_size: 1024
    .name:           _Z7empty_kPi
    .private_segment_fixed_size: 0
    .sgpr_count:     6
    .sgpr_spill_count: 0
    .symbol:         _Z7empty_kPi.kd
    .uniform_work_group_size: 1
    .uses_dynamic_stack: false
    .vgpr_count:     0
    .vgpr_spill_count: 0
    .wavefront_size: 64
  - .agpr_count:     0
    .args:
      - .actual_access:  read_only
        .address_space:  global
        .offset:         0
        .size:           8
        .value_kind:     global_buffer
      - .actual_access:  read_only
        .address_space:  global
        .offset:         8
        .size:           8
        .value_kind:     global_buffer
      - .actual_access:  read_only
        .address_space:  global
        .offset:         16
        .size:           8
        .value_kind:     global_buffer
      - .actual_access:  read_only
        .address_space:  global
        .offset:         24
        .size:           8
        .value_kind:     global_buffer
      - .actual_access:  write_only
        .address_space:  global
        .offset:         32
        .size:           8
        .value_kind:     global_buffer
      - .actual_access:  write_only
        .address_space:  global
        .offset:         40
        .size:           8
        .value_kind:     global_buffer
    .group_segment_fixed_size: 0
    .kernarg_segment_align: 8
    .kernarg_segment_size: 48
    .language:       OpenCL C
    .language_version:
      - 2
      - 0
    .max_flat_workgroup_size: 256
    .name:           _Z4ln_kPKfS0_S0_S0_PfPDF16_
    .private_segment_fixed_size: 0
    .sgpr_count:     19
    .sgpr_spill_count: 0
    .symbol:         _Z4ln_kPKfS0_S0_S0_PfPDF16_.kd
    .uniform_work_group_size: 1
    .uses_dynamic_stack: false
    .vgpr_count:     59
    .vgpr_spill_count: 0
    .wavefront_size: 64
  - .agpr_count:     0
    .args:
      - .actual_access:  read_only
        .address_space:  global
        .offset:         0
        .size:           8
        .value_kind:     global_buffer
      - .actual_access:  read_only
        .address_space:  global
        .offset:         8
        .size:           8
        .value_kind:     global_buffer
      - .actual_access:  read_only
        .address_space:  global
        .offset:         16
        .size:           8
        .value_kind:     global_buffer
      - .actual_access:  read_only
        .address_space:  global
        .offset:         24
        .size:           8
        .value_kind:     global_buffer
      - .actual_access:  read_only
        .address_space:  global
        .offset:         32
        .size:           8
        .value_kind:     global_buffer
      - .actual_access:  write_only
        .address_space:  global
        .offset:         40
        .size:           8
        .value_kind:     global_buffer
      - .actual_access:  write_only
        .address_space:  global
        .offset:         48
        .size:           8
        .value_kind:     global_buffer
      - .actual_access:  write_only
        .address_space:  global
        .offset:         56
        .size:           8
        .value_kind:     global_buffer
      - .actual_access:  write_only
        .address_space:  global
        .offset:         64
        .size:           8
        .value_kind:     global_buffer
      - .offset:         72
        .size:           4
        .value_kind:     by_value
    .group_segment_fixed_size: 24704
    .kernarg_segment_align: 8
    .kernarg_segment_size: 76
    .language:       OpenCL C
    .language_version:
      - 2
      - 0
    .max_flat_workgroup_size: 1024
    .name:           _Z11ln_router_kPKfS0_S0_S0_S0_PfPDF16_PiS1_i
    .private_segment_fixed_size: 0
    .sgpr_count:     34
    .sgpr_spill_count: 0
    .symbol:         _Z11ln_router_kPKfS0_S0_S0_S0_PfPDF16_PiS1_i.kd
    .uniform_work_group_size: 1
    .uses_dynamic_stack: false
    .vgpr_count:     56
    .vgpr_spill_count: 0
    .wavefront_size: 64
  - .agpr_count:     0
    .args:
      - .actual_access:  read_only
        .address_space:  global
        .offset:         0
        .size:           8
        .value_kind:     global_buffer
      - .actual_access:  write_only
        .address_space:  global
        .offset:         8
        .size:           8
        .value_kind:     global_buffer
      - .actual_access:  write_only
        .address_space:  global
        .offset:         16
        .size:           8
        .value_kind:     global_buffer
    .group_segment_fixed_size: 4176
    .kernarg_segment_align: 8
    .kernarg_segment_size: 24
    .language:       OpenCL C
    .language_version:
      - 2
      - 0
    .max_flat_workgroup_size: 1024
    .name:           _Z6sort_kPKiPiS1_
    .private_segment_fixed_size: 0
    .sgpr_count:     102
    .sgpr_spill_count: 0
    .symbol:         _Z6sort_kPKiPiS1_.kd
    .uniform_work_group_size: 1
    .uses_dynamic_stack: false
    .vgpr_count:     48
    .vgpr_spill_count: 0
    .wavefront_size: 64
  - .agpr_count:     0
    .args:
      - .offset:         0
        .size:           272
        .value_kind:     by_value
      - .actual_access:  read_only
        .address_space:  global
        .offset:         272
        .size:           8
        .value_kind:     global_buffer
      - .actual_access:  read_only
        .address_space:  global
        .offset:         280
        .size:           8
        .value_kind:     global_buffer
      - .actual_access:  read_only
        .address_space:  global
        .offset:         288
        .size:           8
        .value_kind:     global_buffer
      - .actual_access:  read_only
        .address_space:  global
        .offset:         296
        .size:           8
        .value_kind:     global_buffer
      - .actual_access:  read_only
        .address_space:  global
        .offset:         304
        .size:           8
        .value_kind:     global_buffer
      - .actual_access:  read_only
        .address_space:  global
        .offset:         312
        .size:           8
        .value_kind:     global_buffer
      - .actual_access:  read_only
        .address_space:  global
        .offset:         320
        .size:           8
        .value_kind:     global_buffer
      - .actual_access:  write_only
        .address_space:  global
        .offset:         328
        .size:           8
        .value_kind:     global_buffer
      - .actual_access:  write_only
        .address_space:  global
        .offset:         336
        .size:           8
        .value_kind:     global_buffer
      - .actual_access:  write_only
        .address_space:  global
        .offset:         344
        .size:           8
        .value_kind:     global_buffer
    .group_segment_fixed_size: 16640
    .kernarg_segment_align: 8
    .kernarg_segment_size: 352
    .language:       OpenCL C
    .language_version:
      - 2
      - 0
    .max_flat_workgroup_size: 256
    .name:           _Z5pre_k7CvtArgsPKiS1_PKfS3_S3_S3_S3_PfPDF16_S4_
    .private_segment_fixed_size: 0
    .sgpr_count:     22
    .sgpr_spill_count: 0
    .symbol:         _Z5pre_k7CvtArgsPKiS1_PKfS3_S3_S3_S3_PfPDF16_S4_.kd
    .uniform_work_group_size: 1
    .uses_dynamic_stack: false
    .vgpr_count:     67
    .vgpr_spill_count: 0
    .wavefront_size: 64
  - .agpr_count:     0
    .args:
      - .actual_access:  read_only
        .address_space:  global
        .offset:         0
        .size:           8
        .value_kind:     global_buffer
      - .actual_access:  read_only
        .address_space:  global
        .offset:         8
        .size:           8
        .value_kind:     global_buffer
      - .actual_access:  read_only
        .address_space:  global
        .offset:         16
        .size:           8
        .value_kind:     global_buffer
      - .actual_access:  read_only
        .address_space:  global
        .offset:         24
        .size:           8
        .value_kind:     global_buffer
      - .actual_access:  write_only
        .address_space:  global
        .offset:         32
        .size:           8
        .value_kind:     global_buffer
      - .actual_access:  read_only
        .address_space:  global
        .offset:         40
        .size:           8
        .value_kind:     global_buffer
      - .offset:         48
        .size:           4
        .value_kind:     by_value
      - .actual_access:  write_only
        .address_space:  global
        .offset:         56
        .size:           8
        .value_kind:     global_buffer
    .group_segment_fixed_size: 133120
    .kernarg_segment_align: 8
    .kernarg_segment_size: 64
    .language:       OpenCL C
    .language_version:
      - 2
      - 0
    .max_flat_workgroup_size: 512
    .name:           _Z6attn_kPKDF16_S0_S0_PKfPDF16_PK15HIP_vector_typeIfLj4EEiPf
    .private_segment_fixed_size: 0
    .sgpr_count:     24
    .sgpr_spill_count: 0
    .symbol:         _Z6attn_kPKDF16_S0_S0_PKfPDF16_PK15HIP_vector_typeIfLj4EEiPf.kd
    .uniform_work_group_size: 1
    .uses_dynamic_stack: false
    .vgpr_count:     110
    .vgpr_spill_count: 0
    .wavefront_size: 64
  - .agpr_count:     0
    .args:
      - .actual_access:  read_only
        .address_space:  global
        .offset:         0
        .size:           8
        .value_kind:     global_buffer
      - .actual_access:  read_only
        .address_space:  global
        .offset:         8
        .size:           8
        .value_kind:     global_buffer
      - .actual_access:  read_only
        .address_space:  global
        .offset:         16
        .size:           8
        .value_kind:     global_buffer
      - .actual_access:  read_only
        .address_space:  global
        .offset:         24
        .size:           8
        .value_kind:     global_buffer
      - .actual_access:  write_only
        .address_space:  global
        .offset:         32
        .size:           8
        .value_kind:     global_buffer
      - .actual_access:  read_only
        .address_space:  global
        .offset:         40
        .size:           8
        .value_kind:     global_buffer
      - .actual_access:  read_only
        .address_space:  global
        .offset:         48
        .size:           8
        .value_kind:     global_buffer
      - .actual_access:  write_only
        .address_space:  global
        .offset:         56
        .size:           8
        .value_kind:     global_buffer
      - .actual_access:  read_only
        .address_space:  global
        .offset:         64
        .size:           8
        .value_kind:     global_buffer
      - .offset:         72
        .size:           4
        .value_kind:     by_value
      - .actual_access:  read_only
        .address_space:  global
        .offset:         80
        .size:           8
        .value_kind:     global_buffer
      - .offset:         88
        .size:           4
        .value_kind:     by_value
      - .actual_access:  write_only
        .address_space:  global
        .offset:         96
        .size:           8
        .value_kind:     global_buffer
    .group_segment_fixed_size: 7168
    .kernarg_segment_align: 8
    .kernarg_segment_size: 104
    .language:       OpenCL C
    .language_version:
      - 2
      - 0
    .max_flat_workgroup_size: 256
    .name:           _Z9tail_up_kPKfPKiS0_S0_PfS0_S2_S3_PK15HIP_vector_typeIfLj4EEiS7_iS3_
    .private_segment_fixed_size: 0
    .sgpr_count:     70
    .sgpr_spill_count: 0
    .symbol:         _Z9tail_up_kPKfPKiS0_S0_PfS0_S2_S3_PK15HIP_vector_typeIfLj4EEiS7_iS3_.kd
    .uniform_work_group_size: 1
    .uses_dynamic_stack: false
    .vgpr_count:     112
    .vgpr_spill_count: 0
    .wavefront_size: 64
  - .agpr_count:     0
    .args:
      - .actual_access:  read_only
        .address_space:  global
        .offset:         0
        .size:           8
        .value_kind:     global_buffer
      - .offset:         8
        .size:           4
        .value_kind:     by_value
      - .actual_access:  read_only
        .address_space:  global
        .offset:         16
        .size:           8
        .value_kind:     global_buffer
      - .actual_access:  read_only
        .address_space:  global
        .offset:         24
        .size:           8
        .value_kind:     global_buffer
      - .actual_access:  read_only
        .address_space:  global
        .offset:         32
        .size:           8
        .value_kind:     global_buffer
      - .actual_access:  read_only
        .address_space:  global
        .offset:         40
        .size:           8
        .value_kind:     global_buffer
      - .actual_access:  write_only
        .address_space:  global
        .offset:         48
        .size:           8
        .value_kind:     global_buffer
    .group_segment_fixed_size: 0
    .kernarg_segment_align: 8
    .kernarg_segment_size: 56
    .language:       OpenCL C
    .language_version:
      - 2
      - 0
    .max_flat_workgroup_size: 512
    .name:           _Z9tail_ln_kPKfiS0_S0_S0_S0_Pf
    .private_segment_fixed_size: 0
    .sgpr_count:     22
    .sgpr_spill_count: 0
    .symbol:         _Z9tail_ln_kPKfiS0_S0_S0_S0_Pf.kd
    .uniform_work_group_size: 1
    .uses_dynamic_stack: false
    .vgpr_count:     48
    .vgpr_spill_count: 0
    .wavefront_size: 64
  - .agpr_count:     0
    .args:
      - .actual_access:  read_only
        .address_space:  global
        .offset:         0
        .size:           8
        .value_kind:     global_buffer
      - .actual_access:  read_only
        .address_space:  global
        .offset:         8
        .size:           8
        .value_kind:     global_buffer
      - .actual_access:  read_only
        .address_space:  global
        .offset:         16
        .size:           8
        .value_kind:     global_buffer
      - .actual_access:  read_only
        .address_space:  global
        .offset:         24
        .size:           8
        .value_kind:     global_buffer
      - .actual_access:  read_only
        .address_space:  global
        .offset:         32
        .size:           8
        .value_kind:     global_buffer
      - .actual_access:  read_only
        .address_space:  global
        .offset:         40
        .size:           8
        .value_kind:     global_buffer
      - .actual_access:  write_only
        .address_space:  global
        .offset:         48
        .size:           8
        .value_kind:     global_buffer
      - .actual_access:  write_only
        .address_space:  global
        .offset:         56
        .size:           8
        .value_kind:     global_buffer
    .group_segment_fixed_size: 47872
    .kernarg_segment_align: 8
    .kernarg_segment_size: 64
    .language:       OpenCL C
    .language_version:
      - 2
      - 0
    .max_flat_workgroup_size: 256
    .name:           _Z6pool_kPKfS0_S0_S0_S0_S0_PfS1_
    .private_segment_fixed_size: 0
    .sgpr_count:     46
    .sgpr_spill_count: 0
    .symbol:         _Z6pool_kPKfS0_S0_S0_S0_S0_PfS1_.kd
    .uniform_work_group_size: 1
    .uses_dynamic_stack: false
    .vgpr_count:     220
    .vgpr_spill_count: 0
    .wavefront_size: 64
  - .agpr_count:     0
    .args:
      - .actual_access:  read_only
        .address_space:  global
        .offset:         0
        .size:           8
        .value_kind:     global_buffer
      - .actual_access:  read_only
        .address_space:  global
        .offset:         8
        .size:           8
        .value_kind:     global_buffer
      - .actual_access:  read_only
        .address_space:  global
        .offset:         16
        .size:           8
        .value_kind:     global_buffer
      - .actual_access:  read_only
        .address_space:  global
        .offset:         24
        .size:           8
        .value_kind:     global_buffer
      - .actual_access:  read_only
        .address_space:  global
        .offset:         32
        .size:           8
        .value_kind:     global_buffer
      - .actual_access:  read_only
        .address_space:  global
        .offset:         40
        .size:           8
        .value_kind:     global_buffer
      - .actual_access:  write_only
        .address_space:  global
        .offset:         48
        .size:           8
        .value_kind:     global_buffer
    .group_segment_fixed_size: 16
    .kernarg_segment_align: 8
    .kernarg_segment_size: 56
    .language:       OpenCL C
    .language_version:
      - 2
      - 0
    .max_flat_workgroup_size: 256
    .name:           _Z8final2_kPKfS0_S0_S0_S0_S0_Pf
    .private_segment_fixed_size: 0
    .sgpr_count:     52
    .sgpr_spill_count: 0
    .symbol:         _Z8final2_kPKfS0_S0_S0_S0_S0_Pf.kd
    .uniform_work_group_size: 1
    .uses_dynamic_stack: false
    .vgpr_count:     67
    .vgpr_spill_count: 0
    .wavefront_size: 64
  - .agpr_count:     0
    .args:
      - .actual_access:  read_only
        .address_space:  global
        .offset:         0
        .size:           8
        .value_kind:     global_buffer
      - .offset:         8
        .size:           4
        .value_kind:     by_value
      - .actual_access:  read_only
        .address_space:  global
        .offset:         16
        .size:           8
        .value_kind:     global_buffer
      - .actual_access:  read_only
        .address_space:  global
        .offset:         24
        .size:           8
        .value_kind:     global_buffer
      - .actual_access:  read_only
        .address_space:  global
        .offset:         32
        .size:           8
        .value_kind:     global_buffer
      - .actual_access:  read_only
        .address_space:  global
        .offset:         40
        .size:           8
        .value_kind:     global_buffer
      - .actual_access:  write_only
        .address_space:  global
        .offset:         48
        .size:           8
        .value_kind:     global_buffer
    .group_segment_fixed_size: 0
    .kernarg_segment_align: 8
    .kernarg_segment_size: 56
    .language:       OpenCL C
    .language_version:
      - 2
      - 0
    .max_flat_workgroup_size: 512
    .name:           _Z7final_kPKfiS0_S0_S0_S0_Pf
    .private_segment_fixed_size: 0
    .sgpr_count:     36
    .sgpr_spill_count: 0
    .symbol:         _Z7final_kPKfiS0_S0_S0_S0_Pf.kd
    .uniform_work_group_size: 1
    .uses_dynamic_stack: false
    .vgpr_count:     20
    .vgpr_spill_count: 0
    .wavefront_size: 64
  - .agpr_count:     0
    .args:
      - .offset:         0
        .size:           136
        .value_kind:     by_value
    .group_segment_fixed_size: 114688
    .kernarg_segment_align: 8
    .kernarg_segment_size: 136
    .language:       OpenCL C
    .language_version:
      - 2
      - 0
    .max_flat_workgroup_size: 512
    .name:           _Z7gemm2_kILi0ELi3ELi1EEv5GArgs
    .private_segment_fixed_size: 0
    .sgpr_count:     43
    .sgpr_spill_count: 0
    .symbol:         _Z7gemm2_kILi0ELi3ELi1EEv5GArgs.kd
    .uniform_work_group_size: 1
    .uses_dynamic_stack: false
    .vgpr_count:     186
    .vgpr_spill_count: 0
    .wavefront_size: 64
  - .agpr_count:     0
    .args:
      - .offset:         0
        .size:           136
        .value_kind:     by_value
    .group_segment_fixed_size: 131072
    .kernarg_segment_align: 8
    .kernarg_segment_size: 136
    .language:       OpenCL C
    .language_version:
      - 2
      - 0
    .max_flat_workgroup_size: 512
    .name:           _Z6gemm_kILi1ELi128ELi4ELi8EEv5GArgs
    .private_segment_fixed_size: 0
    .sgpr_count:     36
    .sgpr_spill_count: 0
    .symbol:         _Z6gemm_kILi1ELi128ELi4ELi8EEv5GArgs.kd
    .uniform_work_group_size: 1
    .uses_dynamic_stack: false
    .vgpr_count:     74
    .vgpr_spill_count: 0
    .wavefront_size: 64
  - .agpr_count:     0
    .args:
      - .offset:         0
        .size:           136
        .value_kind:     by_value
    .group_segment_fixed_size: 81920
    .kernarg_segment_align: 8
    .kernarg_segment_size: 136
    .language:       OpenCL C
    .language_version:
      - 2
      - 0
    .max_flat_workgroup_size: 256
    .name:           _Z6gemm_kILi2ELi128ELi2ELi4EEv5GArgs
    .private_segment_fixed_size: 0
    .sgpr_count:     65
    .sgpr_spill_count: 0
    .symbol:         _Z6gemm_kILi2ELi128ELi2ELi4EEv5GArgs.kd
    .uniform_work_group_size: 1
    .uses_dynamic_stack: false
    .vgpr_count:     194
    .vgpr_spill_count: 0
    .wavefront_size: 64
  - .agpr_count:     0
    .args:
      - .offset:         0
        .size:           136
        .value_kind:     by_value
    .group_segment_fixed_size: 98304
    .kernarg_segment_align: 8
    .kernarg_segment_size: 136
    .language:       OpenCL C
    .language_version:
      - 2
      - 0
    .max_flat_workgroup_size: 512
    .name:           _Z7gemm2_kILi3ELi2ELi2EEv5GArgs
    .private_segment_fixed_size: 0
    .sgpr_count:     36
    .sgpr_spill_count: 0
    .symbol:         _Z7gemm2_kILi3ELi2ELi2EEv5GArgs.kd
    .uniform_work_group_size: 1
    .uses_dynamic_stack: false
    .vgpr_count:     170
    .vgpr_spill_count: 0
    .wavefront_size: 64
  - .agpr_count:     0
    .args:
      - .actual_access:  read_only
        .address_space:  global
        .offset:         0
        .size:           8
        .value_kind:     global_buffer
      - .actual_access:  read_only
        .address_space:  global
        .offset:         8
        .size:           8
        .value_kind:     global_buffer
      - .actual_access:  write_only
        .address_space:  global
        .offset:         16
        .size:           8
        .value_kind:     global_buffer
    .group_segment_fixed_size: 38912
    .kernarg_segment_align: 8
    .kernarg_segment_size: 24
    .language:       OpenCL C
    .language_version:
      - 2
      - 0
    .max_flat_workgroup_size: 256
    .name:           _Z7gemv8_kILi192ELi3072EEvPKfS1_Pf
    .private_segment_fixed_size: 0
    .sgpr_count:     22
    .sgpr_spill_count: 0
    .symbol:         _Z7gemv8_kILi192ELi3072EEvPKfS1_Pf.kd
    .uniform_work_group_size: 1
    .uses_dynamic_stack: false
    .vgpr_count:     127
    .vgpr_spill_count: 0
    .wavefront_size: 64
